# attention softmax bound cached per phase (skips 2 loads + 6-hop reduction per unit); q/k epilogue issues a row's 4 rope loads together; norm2 row sums via DPP
# speedup vs baseline: 1.0100x; 1.0100x over previous
.LBB0_463:
	v_and_b32_e32 v163, 64, v177
	v_mov_b32_e32 v170, v115
	v_mov_b32_e32 v171, v127
	v_xor_b32_e32 v130, 16, v177
	v_add_u32_e32 v163, 64, v163
	v_mov_b32_e32 v168, v114
	v_mov_b32_e32 v169, v126
	v_pk_mul_f32 v[170:171], v[170:171], v[170:171]
	v_cmp_lt_i32_e32 vcc, v130, v163
	v_pk_fma_f32 v[168:169], v[168:169], v[168:169], v[170:171]
	v_mov_b32_e32 v170, v116
	v_mov_b32_e32 v171, v128
	v_cndmask_b32_e32 v130, v177, v130, vcc
	v_pk_fma_f32 v[168:169], v[170:171], v[170:171], v[168:169]
	v_mov_b32_e32 v170, v117
	v_mov_b32_e32 v171, v129
	v_mov_b32_e32 v172, v141
	v_mov_b32_e32 v173, v145
	v_lshlrev_b32_e32 v165, 2, v130
	v_xor_b32_e32 v130, 32, v177
	v_pk_fma_f32 v[168:169], v[170:171], v[170:171], v[168:169]
	v_mov_b32_e32 v170, v140
	v_mov_b32_e32 v171, v144
	v_pk_mul_f32 v[172:173], v[172:173], v[172:173]
	v_cmp_lt_i32_e32 vcc, v130, v163
	v_pk_fma_f32 v[170:171], v[170:171], v[170:171], v[172:173]
	v_mov_b32_e32 v172, v142
	v_mov_b32_e32 v173, v146
	v_cndmask_b32_e32 v130, v177, v130, vcc
	v_pk_fma_f32 v[170:171], v[172:173], v[172:173], v[170:171]
	v_mov_b32_e32 v172, v143
	v_mov_b32_e32 v173, v147
	v_lshlrev_b32_e32 v163, 2, v130
	v_pk_fma_f32 v[170:171], v[172:173], v[172:173], v[170:171]
	v_add_f32_e32 v130, v168, v169
	v_add_f32_e32 v130, v130, v170
	v_add_f32_e32 v130, v130, v171
	ds_bpermute_b32 v167, v165, v130
	v_cndmask_b32_e64 v182, 1.0, v251, s[6:7]
	s_mul_hi_i32 s6, s78, 0x38e38e39
	s_lshr_b32 s7, s6, 31
	s_ashr_i32 s6, s6, 1
	s_waitcnt lgkmcnt(0)
	v_add_f32_e32 v130, v130, v167
	ds_bpermute_b32 v167, v163, v130
	s_add_i32 s6, s6, s7
	s_mul_i32 s6, s6, 9
	s_sub_i32 s6, s78, s6
	s_lshl_b32 s59, s6, 8
	s_waitcnt lgkmcnt(0)
	v_add_f32_e32 v130, v130, v167
	v_fmamk_f32 v130, v130, 0x36800000, v176
	v_cmp_gt_f32_e32 vcc, s25, v130
	v_mul_f32_e32 v167, 0x4b800000, v130
	v_add_u32_e32 v168, s59, v156
	v_cndmask_b32_e32 v130, v130, v167, vcc
	v_rsq_f32_e32 v130, v130
	v_ashrrev_i32_e32 v169, 31, v168
	v_lshlrev_b64 v[168:169], 5, v[168:169]
	s_waitcnt vmcnt(0)
	v_pk_mul_f32 v[16:17], v[182:183], v[16:17] op_sel_hi:[0,1]
	v_mul_f32_e32 v167, 0x45800000, v130
	v_cndmask_b32_e32 v130, v130, v167, vcc
	v_mul_f32_e32 v188, 0x3c800000, v130
	v_pk_mul_f32 v[14:15], v[182:183], v[14:15] op_sel_hi:[0,1]
	s_cmp_lt_i32 s6, 8
	v_or_b32_e32 v168, v168, v158
	v_pk_mul_f32 v[170:171], v[114:115], v[188:189] op_sel_hi:[1,0]
	v_pk_mul_f32 v[172:173], v[116:117], v[188:189] op_sel_hi:[1,0]
	s_cselect_b64 s[78:79], -1, 0
	s_cmp_gt_i32 s6, 7
	v_pk_mul_f32 v[186:187], v[16:17], v[172:173]
	v_pk_mul_f32 v[184:185], v[14:15], v[170:171]
	v_lshl_add_u64 v[190:191], v[168:169], 3, s[14:15]
	s_cbranch_scc1 .LBB0_465
	global_load_dwordx4 v[218:221], v[190:191], off
	global_load_dwordx4 v[222:225], v[190:191], off offset:16
	global_load_dwordx4 v[226:229], v[190:191], off offset:32
	global_load_dwordx4 v[230:233], v[190:191], off offset:48
	s_waitcnt vmcnt(3)
	v_mov_b64_e32 v[168:169], v[218:219]
	v_mov_b64_e32 v[170:171], v[220:221]
	v_pk_mul_f32 v[174:175], v[184:185], v[168:169] op_sel:[1,1] op_sel_hi:[1,0]
	v_mul_f32_e32 v130, v187, v171
	v_pk_mul_f32 v[172:173], v[184:185], v[168:169]
	v_pk_fma_f32 v[184:185], v[184:185], v[168:169], v[174:175] op_sel_hi:[0,1,1]
	v_pk_fma_f32 v[168:169], v[186:187], v[170:171], v[130:131] op_sel_hi:[1,1,0] neg_lo:[0,0,1] neg_hi:[0,0,1]
	v_mul_f32_e32 v130, v187, v170
	v_pk_fma_f32 v[170:171], v[186:187], v[170:171], v[130:131] op_sel:[0,1,0] op_sel_hi:[1,0,0]
	v_sub_f32_e32 v184, v172, v174
	v_mov_b32_e32 v186, v168
	v_mov_b32_e32 v187, v170
.LBB0_465:
	v_mov_b32_e32 v183, v182
	v_mov_b32_e32 v189, v188
	v_mov_b32_e32 v198, v182
	v_mov_b32_e32 v199, v182
	v_mov_b32_e32 v196, v188
	v_mov_b32_e32 v197, v188
	v_pk_mul_f32 v[12:13], v[198:199], v[12:13]
	v_pk_mul_f32 v[10:11], v[182:183], v[10:11]
	v_pk_mul_f32 v[168:169], v[128:129], v[196:197]
	v_pk_mul_f32 v[170:171], v[126:127], v[188:189]
	v_cndmask_b32_e64 v130, 0, 1, s[78:79]
	v_pk_mul_f32 v[192:193], v[12:13], v[168:169]
	v_cmp_ne_u32_e64 s[6:7], 1, v130
	s_andn2_b64 vcc, exec, s[78:79]
	v_pk_mul_f32 v[194:195], v[10:11], v[170:171]
	s_cbranch_vccnz .LBB0_467
	s_waitcnt vmcnt(2)
	v_mov_b64_e32 v[168:169], v[222:223]
	v_mov_b64_e32 v[170:171], v[224:225]
	v_pk_mul_f32 v[174:175], v[194:195], v[168:169] op_sel:[1,1] op_sel_hi:[1,0]
	v_mul_f32_e32 v130, v193, v171
	v_pk_mul_f32 v[172:173], v[194:195], v[168:169]
	v_pk_fma_f32 v[194:195], v[194:195], v[168:169], v[174:175] op_sel_hi:[0,1,1]
	v_pk_fma_f32 v[168:169], v[192:193], v[170:171], v[130:131] op_sel_hi:[1,1,0] neg_lo:[0,0,1] neg_hi:[0,0,1]
	v_mul_f32_e32 v130, v193, v170
	v_pk_fma_f32 v[170:171], v[192:193], v[170:171], v[130:131] op_sel:[0,1,0] op_sel_hi:[1,0,0]
	v_sub_f32_e32 v194, v172, v174
	v_mov_b32_e32 v192, v168
	v_mov_b32_e32 v193, v170
.LBB0_467:
	v_pk_mul_f32 v[8:9], v[198:199], v[8:9]
	v_pk_mul_f32 v[6:7], v[182:183], v[6:7]
	v_pk_mul_f32 v[168:169], v[142:143], v[196:197]
	v_pk_mul_f32 v[170:171], v[140:141], v[188:189]
	v_pk_mul_f32 v[196:197], v[8:9], v[168:169]
	s_and_b64 vcc, exec, s[6:7]
	v_pk_mul_f32 v[198:199], v[6:7], v[170:171]
	s_cbranch_vccnz .LBB0_469
	s_waitcnt vmcnt(1)
	v_mov_b64_e32 v[168:169], v[226:227]
	v_mov_b64_e32 v[170:171], v[228:229]
	v_pk_mul_f32 v[174:175], v[198:199], v[168:169] op_sel:[1,1] op_sel_hi:[1,0]
	v_mul_f32_e32 v130, v197, v171
	v_pk_mul_f32 v[172:173], v[198:199], v[168:169]
	v_pk_fma_f32 v[198:199], v[198:199], v[168:169], v[174:175] op_sel_hi:[0,1,1]
	v_pk_fma_f32 v[168:169], v[196:197], v[170:171], v[130:131] op_sel_hi:[1,1,0] neg_lo:[0,0,1] neg_hi:[0,0,1]
	v_mul_f32_e32 v130, v197, v170
	v_pk_fma_f32 v[170:171], v[196:197], v[170:171], v[130:131] op_sel:[0,1,0] op_sel_hi:[1,0,0]
	v_sub_f32_e32 v198, v172, v174
	v_mov_b32_e32 v196, v168
	v_mov_b32_e32 v197, v170
.LBB0_469:
	v_mov_b32_e32 v168, v182
	v_mov_b32_e32 v169, v182
	v_pk_mul_f32 v[4:5], v[168:169], v[4:5]
	v_mov_b32_e32 v168, v188
	v_mov_b32_e32 v169, v188
	v_pk_mul_f32 v[2:3], v[182:183], v[2:3]
	v_pk_mul_f32 v[168:169], v[146:147], v[168:169]
	v_pk_mul_f32 v[170:171], v[144:145], v[188:189]
	v_pk_mul_f32 v[188:189], v[4:5], v[168:169]
	s_and_b64 vcc, exec, s[6:7]
	v_pk_mul_f32 v[200:201], v[2:3], v[170:171]
	s_cbranch_vccnz .LBB0_471
	s_waitcnt vmcnt(0)
	v_mov_b64_e32 v[168:169], v[230:231]
	v_mov_b64_e32 v[170:171], v[232:233]
	v_pk_mul_f32 v[174:175], v[200:201], v[168:169] op_sel:[1,1] op_sel_hi:[1,0]
	v_mul_f32_e32 v130, v189, v171
	v_pk_mul_f32 v[172:173], v[200:201], v[168:169]
	v_pk_fma_f32 v[200:201], v[200:201], v[168:169], v[174:175] op_sel_hi:[0,1,1]
	v_pk_fma_f32 v[168:169], v[188:189], v[170:171], v[130:131] op_sel_hi:[1,1,0] neg_lo:[0,0,1] neg_hi:[0,0,1]
	v_mul_f32_e32 v130, v189, v170
	v_pk_fma_f32 v[170:171], v[188:189], v[170:171], v[130:131] op_sel:[0,1,0] op_sel_hi:[1,0,0]
	v_sub_f32_e32 v200, v172, v174
	v_mov_b32_e32 v188, v168
	v_mov_b32_e32 v189, v170
.LBB0_471:
	v_lshlrev_b32_e32 v130, 1, v160
	v_lshl_add_u64 v[182:183], s[82:83], 0, v[130:131]
	v_mad_i64_i32 v[172:173], s[60:61], s76, v156, 0
	v_cvt_pk_bf16_f32 v168, v184, v185
	v_cvt_pk_bf16_f32 v169, v186, v187
	v_cvt_pk_bf16_f32 v170, v194, v195
	v_cvt_pk_bf16_f32 v171, v192, v193
	v_lshl_add_u64 v[172:173], v[172:173], 1, v[182:183]
	global_store_dwordx4 v[172:173], v[168:171], off
	s_nop 1
	v_cvt_pk_bf16_f32 v168, v198, v199
	v_cvt_pk_bf16_f32 v169, v196, v197
	v_cvt_pk_bf16_f32 v170, v200, v201
	v_cvt_pk_bf16_f32 v171, v188, v189
	global_store_dwordx4 v[172:173], v[168:171], off offset:16
	v_mov_b32_e32 v172, v137
	v_mov_b32_e32 v173, v133
	v_mov_b32_e32 v170, v103
	v_mov_b32_e32 v171, v99
	v_mov_b32_e32 v168, v102
	v_mov_b32_e32 v169, v98
	v_pk_mul_f32 v[170:171], v[170:171], v[170:171]
	v_pk_mul_f32 v[172:173], v[172:173], v[172:173]
	v_pk_fma_f32 v[168:169], v[168:169], v[168:169], v[170:171]
	v_mov_b32_e32 v170, v104
	v_mov_b32_e32 v171, v100
	v_pk_fma_f32 v[168:169], v[170:171], v[170:171], v[168:169]
	v_mov_b32_e32 v170, v105
	v_mov_b32_e32 v171, v101
	v_pk_fma_f32 v[168:169], v[170:171], v[170:171], v[168:169]
	v_mov_b32_e32 v170, v136
	v_mov_b32_e32 v171, v132
	v_pk_fma_f32 v[170:171], v[170:171], v[170:171], v[172:173]
	v_mov_b32_e32 v172, v138
	v_mov_b32_e32 v173, v134
	v_pk_fma_f32 v[170:171], v[172:173], v[172:173], v[170:171]
	v_mov_b32_e32 v172, v139
	v_mov_b32_e32 v173, v135
	v_pk_fma_f32 v[170:171], v[172:173], v[172:173], v[170:171]
	v_add_f32_e32 v130, v168, v169
	v_add_f32_e32 v130, v130, v170
	v_add_f32_e32 v130, v130, v171
	ds_bpermute_b32 v167, v165, v130
	v_add_u32_e32 v168, s59, v162
	v_ashrrev_i32_e32 v169, 31, v168
	v_lshlrev_b64 v[168:169], 5, v[168:169]
	v_or_b32_e32 v168, v168, v158
	s_waitcnt lgkmcnt(0)
	v_add_f32_e32 v130, v130, v167
	ds_bpermute_b32 v167, v163, v130
	v_lshl_add_u64 v[190:191], v[168:169], 3, s[14:15]
	s_waitcnt lgkmcnt(0)
	v_add_f32_e32 v130, v130, v167
	v_fmamk_f32 v130, v130, 0x36800000, v176
	v_cmp_gt_f32_e32 vcc, s25, v130
	v_mul_f32_e32 v167, 0x4b800000, v130
	s_nop 0
	v_cndmask_b32_e32 v130, v130, v167, vcc
	v_rsq_f32_e32 v130, v130
	s_nop 0
	v_mul_f32_e32 v167, 0x45800000, v130
	v_cndmask_b32_e32 v130, v130, v167, vcc
	v_mul_f32_e32 v188, 0x3c800000, v130
	v_pk_mul_f32 v[170:171], v[102:103], v[188:189] op_sel_hi:[1,0]
	v_pk_mul_f32 v[172:173], v[104:105], v[188:189] op_sel_hi:[1,0]
	v_pk_mul_f32 v[184:185], v[14:15], v[170:171]
	v_pk_mul_f32 v[186:187], v[16:17], v[172:173]
	s_and_b64 vcc, exec, s[6:7]
	s_cbranch_vccnz .LBB0_473
	global_load_dwordx4 v[218:221], v[190:191], off
	global_load_dwordx4 v[222:225], v[190:191], off offset:16
	global_load_dwordx4 v[226:229], v[190:191], off offset:32
	global_load_dwordx4 v[230:233], v[190:191], off offset:48
	s_waitcnt vmcnt(3)
	v_mov_b64_e32 v[168:169], v[218:219]
	v_mov_b64_e32 v[170:171], v[220:221]
	v_pk_mul_f32 v[174:175], v[184:185], v[168:169] op_sel:[1,1] op_sel_hi:[1,0]
	v_mul_f32_e32 v130, v187, v171
	v_pk_mul_f32 v[172:173], v[184:185], v[168:169]
	v_pk_fma_f32 v[184:185], v[184:185], v[168:169], v[174:175] op_sel_hi:[0,1,1]
	v_pk_fma_f32 v[168:169], v[186:187], v[170:171], v[130:131] op_sel_hi:[1,1,0] neg_lo:[0,0,1] neg_hi:[0,0,1]
	v_mul_f32_e32 v130, v187, v170
	v_pk_fma_f32 v[170:171], v[186:187], v[170:171], v[130:131] op_sel:[0,1,0] op_sel_hi:[1,0,0]
	v_sub_f32_e32 v184, v172, v174
	v_mov_b32_e32 v186, v168
	v_mov_b32_e32 v187, v170
.LBB0_473:
	v_mov_b32_e32 v189, v188
	v_mov_b32_e32 v196, v188
	v_mov_b32_e32 v197, v188
	v_pk_mul_f32 v[168:169], v[100:101], v[196:197]
	v_pk_mul_f32 v[170:171], v[98:99], v[188:189]
	v_pk_mul_f32 v[192:193], v[12:13], v[168:169]
	s_and_b64 vcc, exec, s[6:7]
	v_pk_mul_f32 v[194:195], v[10:11], v[170:171]
	s_cbranch_vccnz .LBB0_475
	s_waitcnt vmcnt(2)
	v_mov_b64_e32 v[168:169], v[222:223]
	v_mov_b64_e32 v[170:171], v[224:225]
	v_pk_mul_f32 v[174:175], v[194:195], v[168:169] op_sel:[1,1] op_sel_hi:[1,0]
	v_mul_f32_e32 v130, v193, v171
	v_pk_mul_f32 v[172:173], v[194:195], v[168:169]
	v_pk_fma_f32 v[194:195], v[194:195], v[168:169], v[174:175] op_sel_hi:[0,1,1]
	v_pk_fma_f32 v[168:169], v[192:193], v[170:171], v[130:131] op_sel_hi:[1,1,0] neg_lo:[0,0,1] neg_hi:[0,0,1]
	v_mul_f32_e32 v130, v193, v170
	v_pk_fma_f32 v[170:171], v[192:193], v[170:171], v[130:131] op_sel:[0,1,0] op_sel_hi:[1,0,0]
	v_sub_f32_e32 v194, v172, v174
	v_mov_b32_e32 v192, v168
	v_mov_b32_e32 v193, v170
.LBB0_475:
	v_pk_mul_f32 v[168:169], v[138:139], v[196:197]
	v_pk_mul_f32 v[170:171], v[136:137], v[188:189]
	v_pk_mul_f32 v[196:197], v[8:9], v[168:169]
	s_and_b64 vcc, exec, s[6:7]
	v_pk_mul_f32 v[198:199], v[6:7], v[170:171]
	s_cbranch_vccnz .LBB0_477
	s_waitcnt vmcnt(1)
	v_mov_b64_e32 v[168:169], v[226:227]
	v_mov_b64_e32 v[170:171], v[228:229]
	v_pk_mul_f32 v[174:175], v[198:199], v[168:169] op_sel:[1,1] op_sel_hi:[1,0]
	v_mul_f32_e32 v130, v197, v171
	v_pk_mul_f32 v[172:173], v[198:199], v[168:169]
	v_pk_fma_f32 v[198:199], v[198:199], v[168:169], v[174:175] op_sel_hi:[0,1,1]
	v_pk_fma_f32 v[168:169], v[196:197], v[170:171], v[130:131] op_sel_hi:[1,1,0] neg_lo:[0,0,1] neg_hi:[0,0,1]
	v_mul_f32_e32 v130, v197, v170
	v_pk_fma_f32 v[170:171], v[196:197], v[170:171], v[130:131] op_sel:[0,1,0] op_sel_hi:[1,0,0]
	v_sub_f32_e32 v198, v172, v174
	v_mov_b32_e32 v196, v168
	v_mov_b32_e32 v197, v170
.LBB0_477:
	v_mov_b32_e32 v168, v188
	v_mov_b32_e32 v169, v188
	v_pk_mul_f32 v[168:169], v[134:135], v[168:169]
	v_pk_mul_f32 v[170:171], v[132:133], v[188:189]
	v_pk_mul_f32 v[188:189], v[4:5], v[168:169]
	s_and_b64 vcc, exec, s[6:7]
	v_pk_mul_f32 v[200:201], v[2:3], v[170:171]
	s_cbranch_vccnz .LBB0_479
	s_waitcnt vmcnt(0)
	v_mov_b64_e32 v[168:169], v[230:231]
	v_mov_b64_e32 v[170:171], v[232:233]
	v_pk_mul_f32 v[174:175], v[200:201], v[168:169] op_sel:[1,1] op_sel_hi:[1,0]
	v_mul_f32_e32 v130, v189, v171
	v_pk_mul_f32 v[172:173], v[200:201], v[168:169]
	v_pk_fma_f32 v[200:201], v[200:201], v[168:169], v[174:175] op_sel_hi:[0,1,1]
	v_pk_fma_f32 v[168:169], v[188:189], v[170:171], v[130:131] op_sel_hi:[1,1,0] neg_lo:[0,0,1] neg_hi:[0,0,1]
	v_mul_f32_e32 v130, v189, v170
	v_pk_fma_f32 v[170:171], v[188:189], v[170:171], v[130:131] op_sel:[0,1,0] op_sel_hi:[1,0,0]
	v_sub_f32_e32 v200, v172, v174
	v_mov_b32_e32 v188, v168
	v_mov_b32_e32 v189, v170
.LBB0_479:
	v_mad_i64_i32 v[172:173], s[60:61], s76, v162, 0
	v_cvt_pk_bf16_f32 v168, v184, v185
	v_cvt_pk_bf16_f32 v169, v186, v187
	v_cvt_pk_bf16_f32 v170, v194, v195
	v_cvt_pk_bf16_f32 v171, v192, v193
	v_lshl_add_u64 v[172:173], v[172:173], 1, v[182:183]
	global_store_dwordx4 v[172:173], v[168:171], off
	s_nop 1
	v_cvt_pk_bf16_f32 v168, v198, v199
	v_cvt_pk_bf16_f32 v169, v196, v197
	v_cvt_pk_bf16_f32 v170, v200, v201
	v_cvt_pk_bf16_f32 v171, v188, v189
	global_store_dwordx4 v[172:173], v[168:171], off offset:16
	v_mov_b32_e32 v172, v111
	v_mov_b32_e32 v173, v107
	v_mov_b32_e32 v170, v79
	v_mov_b32_e32 v171, v71
	v_mov_b32_e32 v168, v78
	v_mov_b32_e32 v169, v70
	v_pk_mul_f32 v[170:171], v[170:171], v[170:171]
	v_pk_mul_f32 v[172:173], v[172:173], v[172:173]
	v_pk_fma_f32 v[168:169], v[168:169], v[168:169], v[170:171]
	v_mov_b32_e32 v170, v80
	v_mov_b32_e32 v171, v72
	v_pk_fma_f32 v[168:169], v[170:171], v[170:171], v[168:169]
	v_mov_b32_e32 v170, v81
	v_mov_b32_e32 v171, v73
	v_pk_fma_f32 v[168:169], v[170:171], v[170:171], v[168:169]
	v_mov_b32_e32 v170, v110
	v_mov_b32_e32 v171, v106
	v_pk_fma_f32 v[170:171], v[170:171], v[170:171], v[172:173]
	v_mov_b32_e32 v172, v112
	v_mov_b32_e32 v173, v108
	v_pk_fma_f32 v[170:171], v[172:173], v[172:173], v[170:171]
	v_mov_b32_e32 v172, v113
	v_mov_b32_e32 v173, v109
	v_pk_fma_f32 v[170:171], v[172:173], v[172:173], v[170:171]
	v_add_f32_e32 v130, v168, v169
	v_add_f32_e32 v130, v130, v170
	v_add_f32_e32 v130, v130, v171
	ds_bpermute_b32 v167, v165, v130
	v_add_u32_e32 v168, s59, v164
	v_ashrrev_i32_e32 v169, 31, v168
	v_lshlrev_b64 v[168:169], 5, v[168:169]
	v_or_b32_e32 v168, v168, v158
	s_waitcnt lgkmcnt(0)
	v_add_f32_e32 v130, v130, v167
	ds_bpermute_b32 v167, v163, v130
	v_lshl_add_u64 v[190:191], v[168:169], 3, s[14:15]
	s_waitcnt lgkmcnt(0)
	v_add_f32_e32 v130, v130, v167
	v_fmamk_f32 v130, v130, 0x36800000, v176
	v_cmp_gt_f32_e32 vcc, s25, v130
	v_mul_f32_e32 v167, 0x4b800000, v130
	s_nop 0
	v_cndmask_b32_e32 v130, v130, v167, vcc
	v_rsq_f32_e32 v130, v130
	s_nop 0
	v_mul_f32_e32 v167, 0x45800000, v130
	v_cndmask_b32_e32 v130, v130, v167, vcc
	v_mul_f32_e32 v188, 0x3c800000, v130
	v_pk_mul_f32 v[170:171], v[78:79], v[188:189] op_sel_hi:[1,0]
	v_pk_mul_f32 v[172:173], v[80:81], v[188:189] op_sel_hi:[1,0]
	v_pk_mul_f32 v[184:185], v[14:15], v[170:171]
	v_pk_mul_f32 v[186:187], v[16:17], v[172:173]
	s_and_b64 vcc, exec, s[6:7]
	s_cbranch_vccnz .LBB0_481
	global_load_dwordx4 v[218:221], v[190:191], off
	global_load_dwordx4 v[222:225], v[190:191], off offset:16
	global_load_dwordx4 v[226:229], v[190:191], off offset:32
	global_load_dwordx4 v[230:233], v[190:191], off offset:48
	s_waitcnt vmcnt(3)
	v_mov_b64_e32 v[168:169], v[218:219]
	v_mov_b64_e32 v[170:171], v[220:221]
	v_pk_mul_f32 v[174:175], v[184:185], v[168:169] op_sel:[1,1] op_sel_hi:[1,0]
	v_mul_f32_e32 v130, v187, v171
	v_pk_mul_f32 v[172:173], v[184:185], v[168:169]
	v_pk_fma_f32 v[184:185], v[184:185], v[168:169], v[174:175] op_sel_hi:[0,1,1]
	v_pk_fma_f32 v[168:169], v[186:187], v[170:171], v[130:131] op_sel_hi:[1,1,0] neg_lo:[0,0,1] neg_hi:[0,0,1]
	v_mul_f32_e32 v130, v187, v170
	v_pk_fma_f32 v[170:171], v[186:187], v[170:171], v[130:131] op_sel:[0,1,0] op_sel_hi:[1,0,0]
	v_sub_f32_e32 v184, v172, v174
	v_mov_b32_e32 v186, v168
	v_mov_b32_e32 v187, v170
.LBB0_481:
	v_mov_b32_e32 v189, v188
	v_mov_b32_e32 v196, v188
	v_mov_b32_e32 v197, v188
	v_pk_mul_f32 v[168:169], v[72:73], v[196:197]
	v_pk_mul_f32 v[170:171], v[70:71], v[188:189]
	v_pk_mul_f32 v[192:193], v[12:13], v[168:169]
	s_and_b64 vcc, exec, s[6:7]
	v_pk_mul_f32 v[194:195], v[10:11], v[170:171]
	s_cbranch_vccnz .LBB0_483
	s_waitcnt vmcnt(2)
	v_mov_b64_e32 v[168:169], v[222:223]
	v_mov_b64_e32 v[170:171], v[224:225]
	v_pk_mul_f32 v[174:175], v[194:195], v[168:169] op_sel:[1,1] op_sel_hi:[1,0]
	v_mul_f32_e32 v130, v193, v171
	v_pk_mul_f32 v[172:173], v[194:195], v[168:169]
	v_pk_fma_f32 v[194:195], v[194:195], v[168:169], v[174:175] op_sel_hi:[0,1,1]
	v_pk_fma_f32 v[168:169], v[192:193], v[170:171], v[130:131] op_sel_hi:[1,1,0] neg_lo:[0,0,1] neg_hi:[0,0,1]
	v_mul_f32_e32 v130, v193, v170
	v_pk_fma_f32 v[170:171], v[192:193], v[170:171], v[130:131] op_sel:[0,1,0] op_sel_hi:[1,0,0]
	v_sub_f32_e32 v194, v172, v174
	v_mov_b32_e32 v192, v168
	v_mov_b32_e32 v193, v170
.LBB0_483:
	v_pk_mul_f32 v[168:169], v[112:113], v[196:197]
	v_pk_mul_f32 v[170:171], v[110:111], v[188:189]
	v_pk_mul_f32 v[196:197], v[8:9], v[168:169]
	s_and_b64 vcc, exec, s[6:7]
	v_pk_mul_f32 v[198:199], v[6:7], v[170:171]
	s_cbranch_vccnz .LBB0_485
	s_waitcnt vmcnt(1)
	v_mov_b64_e32 v[168:169], v[226:227]
	v_mov_b64_e32 v[170:171], v[228:229]
	v_pk_mul_f32 v[174:175], v[198:199], v[168:169] op_sel:[1,1] op_sel_hi:[1,0]
	v_mul_f32_e32 v130, v197, v171
	v_pk_mul_f32 v[172:173], v[198:199], v[168:169]
	v_pk_fma_f32 v[198:199], v[198:199], v[168:169], v[174:175] op_sel_hi:[0,1,1]
	v_pk_fma_f32 v[168:169], v[196:197], v[170:171], v[130:131] op_sel_hi:[1,1,0] neg_lo:[0,0,1] neg_hi:[0,0,1]
	v_mul_f32_e32 v130, v197, v170
	v_pk_fma_f32 v[170:171], v[196:197], v[170:171], v[130:131] op_sel:[0,1,0] op_sel_hi:[1,0,0]
	v_sub_f32_e32 v198, v172, v174
	v_mov_b32_e32 v196, v168
	v_mov_b32_e32 v197, v170
.LBB0_485:
	v_mov_b32_e32 v168, v188
	v_mov_b32_e32 v169, v188
	v_pk_mul_f32 v[168:169], v[108:109], v[168:169]
	v_pk_mul_f32 v[170:171], v[106:107], v[188:189]
	v_pk_mul_f32 v[188:189], v[4:5], v[168:169]
	s_and_b64 vcc, exec, s[6:7]
	v_pk_mul_f32 v[200:201], v[2:3], v[170:171]
	s_cbranch_vccnz .LBB0_487
	s_waitcnt vmcnt(0)
	v_mov_b64_e32 v[168:169], v[230:231]
	v_mov_b64_e32 v[170:171], v[232:233]
	v_pk_mul_f32 v[174:175], v[200:201], v[168:169] op_sel:[1,1] op_sel_hi:[1,0]
	v_mul_f32_e32 v130, v189, v171
	v_pk_mul_f32 v[172:173], v[200:201], v[168:169]
	v_pk_fma_f32 v[200:201], v[200:201], v[168:169], v[174:175] op_sel_hi:[0,1,1]
	v_pk_fma_f32 v[168:169], v[188:189], v[170:171], v[130:131] op_sel_hi:[1,1,0] neg_lo:[0,0,1] neg_hi:[0,0,1]
	v_mul_f32_e32 v130, v189, v170
	v_pk_fma_f32 v[170:171], v[188:189], v[170:171], v[130:131] op_sel:[0,1,0] op_sel_hi:[1,0,0]
	v_sub_f32_e32 v200, v172, v174
	v_mov_b32_e32 v188, v168
	v_mov_b32_e32 v189, v170
.LBB0_487:
	v_mad_i64_i32 v[172:173], s[60:61], s76, v164, 0
	v_cvt_pk_bf16_f32 v168, v184, v185
	v_cvt_pk_bf16_f32 v169, v186, v187
	v_cvt_pk_bf16_f32 v170, v194, v195
	v_cvt_pk_bf16_f32 v171, v192, v193
	v_lshl_add_u64 v[172:173], v[172:173], 1, v[182:183]
	global_store_dwordx4 v[172:173], v[168:171], off
	s_nop 1
	v_cvt_pk_bf16_f32 v168, v198, v199
	v_cvt_pk_bf16_f32 v169, v196, v197
	v_cvt_pk_bf16_f32 v170, v200, v201
	v_cvt_pk_bf16_f32 v171, v188, v189
	global_store_dwordx4 v[172:173], v[168:171], off offset:16
	v_mov_b32_e32 v172, v75
	v_mov_b32_e32 v173, v67
	v_mov_b32_e32 v170, v51
	v_mov_b32_e32 v171, v43
	v_mov_b32_e32 v168, v50
	v_mov_b32_e32 v169, v42
	v_pk_mul_f32 v[170:171], v[170:171], v[170:171]
	v_pk_mul_f32 v[172:173], v[172:173], v[172:173]
	v_pk_fma_f32 v[168:169], v[168:169], v[168:169], v[170:171]
	v_mov_b32_e32 v170, v52
	v_mov_b32_e32 v171, v44
	v_pk_fma_f32 v[168:169], v[170:171], v[170:171], v[168:169]
	v_mov_b32_e32 v170, v53
	v_mov_b32_e32 v171, v45
	v_pk_fma_f32 v[168:169], v[170:171], v[170:171], v[168:169]
	v_mov_b32_e32 v170, v74
	v_mov_b32_e32 v171, v66
	v_pk_fma_f32 v[170:171], v[170:171], v[170:171], v[172:173]
	v_mov_b32_e32 v172, v76
	v_mov_b32_e32 v173, v68
	v_pk_fma_f32 v[170:171], v[172:173], v[172:173], v[170:171]
	v_mov_b32_e32 v172, v77
	v_mov_b32_e32 v173, v69
	v_pk_fma_f32 v[170:171], v[172:173], v[172:173], v[170:171]
	v_add_f32_e32 v130, v168, v169
	v_add_f32_e32 v130, v130, v170
	v_add_f32_e32 v130, v130, v171
	ds_bpermute_b32 v167, v165, v130
	v_add_u32_e32 v168, s59, v166
	v_ashrrev_i32_e32 v169, 31, v168
	v_lshlrev_b64 v[168:169], 5, v[168:169]
	v_or_b32_e32 v168, v168, v158
	s_waitcnt lgkmcnt(0)
	v_add_f32_e32 v130, v130, v167
	ds_bpermute_b32 v167, v163, v130
	v_lshl_add_u64 v[190:191], v[168:169], 3, s[14:15]
	s_waitcnt lgkmcnt(0)
	v_add_f32_e32 v130, v130, v167
	v_fmamk_f32 v130, v130, 0x36800000, v176
	v_cmp_gt_f32_e32 vcc, s25, v130
	v_mul_f32_e32 v167, 0x4b800000, v130
	s_nop 0
	v_cndmask_b32_e32 v130, v130, v167, vcc
	v_rsq_f32_e32 v130, v130
	s_nop 0
	v_mul_f32_e32 v167, 0x45800000, v130
	v_cndmask_b32_e32 v130, v130, v167, vcc
	v_mul_f32_e32 v188, 0x3c800000, v130
	v_pk_mul_f32 v[170:171], v[50:51], v[188:189] op_sel_hi:[1,0]
	v_pk_mul_f32 v[172:173], v[52:53], v[188:189] op_sel_hi:[1,0]
	v_pk_mul_f32 v[184:185], v[14:15], v[170:171]
	v_pk_mul_f32 v[186:187], v[16:17], v[172:173]
	s_and_b64 vcc, exec, s[6:7]
	s_cbranch_vccnz .LBB0_489
	global_load_dwordx4 v[218:221], v[190:191], off
	global_load_dwordx4 v[222:225], v[190:191], off offset:16
	global_load_dwordx4 v[226:229], v[190:191], off offset:32
	global_load_dwordx4 v[230:233], v[190:191], off offset:48
	s_waitcnt vmcnt(3)
	v_mov_b64_e32 v[168:169], v[218:219]
	v_mov_b64_e32 v[170:171], v[220:221]
	v_pk_mul_f32 v[174:175], v[184:185], v[168:169] op_sel:[1,1] op_sel_hi:[1,0]
	v_mul_f32_e32 v130, v187, v171
	v_pk_mul_f32 v[172:173], v[184:185], v[168:169]
	v_pk_fma_f32 v[184:185], v[184:185], v[168:169], v[174:175] op_sel_hi:[0,1,1]
	v_pk_fma_f32 v[168:169], v[186:187], v[170:171], v[130:131] op_sel_hi:[1,1,0] neg_lo:[0,0,1] neg_hi:[0,0,1]
	v_mul_f32_e32 v130, v187, v170
	v_pk_fma_f32 v[170:171], v[186:187], v[170:171], v[130:131] op_sel:[0,1,0] op_sel_hi:[1,0,0]
	v_sub_f32_e32 v184, v172, v174
	v_mov_b32_e32 v186, v168
	v_mov_b32_e32 v187, v170
.LBB0_489:
	v_mov_b32_e32 v189, v188
	v_mov_b32_e32 v196, v188
	v_mov_b32_e32 v197, v188
	v_pk_mul_f32 v[168:169], v[44:45], v[196:197]
	v_pk_mul_f32 v[170:171], v[42:43], v[188:189]
	v_pk_mul_f32 v[192:193], v[12:13], v[168:169]
	s_and_b64 vcc, exec, s[6:7]
	v_pk_mul_f32 v[194:195], v[10:11], v[170:171]
	s_cbranch_vccnz .LBB0_491
	s_waitcnt vmcnt(2)
	v_mov_b64_e32 v[168:169], v[222:223]
	v_mov_b64_e32 v[170:171], v[224:225]
	v_pk_mul_f32 v[174:175], v[194:195], v[168:169] op_sel:[1,1] op_sel_hi:[1,0]
	v_mul_f32_e32 v130, v193, v171
	v_pk_mul_f32 v[172:173], v[194:195], v[168:169]
	v_pk_fma_f32 v[194:195], v[194:195], v[168:169], v[174:175] op_sel_hi:[0,1,1]
	v_pk_fma_f32 v[168:169], v[192:193], v[170:171], v[130:131] op_sel_hi:[1,1,0] neg_lo:[0,0,1] neg_hi:[0,0,1]
	v_mul_f32_e32 v130, v193, v170
	v_pk_fma_f32 v[170:171], v[192:193], v[170:171], v[130:131] op_sel:[0,1,0] op_sel_hi:[1,0,0]
	v_sub_f32_e32 v194, v172, v174
	v_mov_b32_e32 v192, v168
	v_mov_b32_e32 v193, v170
.LBB0_491:
	v_pk_mul_f32 v[168:169], v[76:77], v[196:197]
	v_pk_mul_f32 v[170:171], v[74:75], v[188:189]
	v_pk_mul_f32 v[196:197], v[8:9], v[168:169]
	s_and_b64 vcc, exec, s[6:7]
	v_pk_mul_f32 v[198:199], v[6:7], v[170:171]
	s_cbranch_vccnz .LBB0_493
	s_waitcnt vmcnt(1)
	v_mov_b64_e32 v[168:169], v[226:227]
	v_mov_b64_e32 v[170:171], v[228:229]
	v_pk_mul_f32 v[174:175], v[198:199], v[168:169] op_sel:[1,1] op_sel_hi:[1,0]
	v_mul_f32_e32 v130, v197, v171
	v_pk_mul_f32 v[172:173], v[198:199], v[168:169]
	v_pk_fma_f32 v[198:199], v[198:199], v[168:169], v[174:175] op_sel_hi:[0,1,1]
	v_pk_fma_f32 v[168:169], v[196:197], v[170:171], v[130:131] op_sel_hi:[1,1,0] neg_lo:[0,0,1] neg_hi:[0,0,1]
	v_mul_f32_e32 v130, v197, v170
	v_pk_fma_f32 v[170:171], v[196:197], v[170:171], v[130:131] op_sel:[0,1,0] op_sel_hi:[1,0,0]
	v_sub_f32_e32 v198, v172, v174
	v_mov_b32_e32 v196, v168
	v_mov_b32_e32 v197, v170
.LBB0_493:
	v_mov_b32_e32 v168, v188
	v_mov_b32_e32 v169, v188
	v_pk_mul_f32 v[168:169], v[68:69], v[168:169]
	v_pk_mul_f32 v[170:171], v[66:67], v[188:189]
	v_pk_mul_f32 v[188:189], v[4:5], v[168:169]
	s_and_b64 vcc, exec, s[6:7]
	v_pk_mul_f32 v[200:201], v[2:3], v[170:171]
	s_cbranch_vccnz .LBB0_495
	s_waitcnt vmcnt(0)
	v_mov_b64_e32 v[168:169], v[230:231]
	v_mov_b64_e32 v[170:171], v[232:233]
	v_pk_mul_f32 v[174:175], v[200:201], v[168:169] op_sel:[1,1] op_sel_hi:[1,0]
	v_mul_f32_e32 v130, v189, v171
	v_pk_mul_f32 v[172:173], v[200:201], v[168:169]
	v_pk_fma_f32 v[200:201], v[200:201], v[168:169], v[174:175] op_sel_hi:[0,1,1]
	v_pk_fma_f32 v[168:169], v[188:189], v[170:171], v[130:131] op_sel_hi:[1,1,0] neg_lo:[0,0,1] neg_hi:[0,0,1]
	v_mul_f32_e32 v130, v189, v170
	v_pk_fma_f32 v[170:171], v[188:189], v[170:171], v[130:131] op_sel:[0,1,0] op_sel_hi:[1,0,0]
	v_sub_f32_e32 v200, v172, v174
	v_mov_b32_e32 v188, v168
	v_mov_b32_e32 v189, v170
.LBB0_495:
	v_mad_i64_i32 v[172:173], s[60:61], s76, v166, 0
	v_cvt_pk_bf16_f32 v168, v184, v185
	v_cvt_pk_bf16_f32 v169, v186, v187
	v_cvt_pk_bf16_f32 v170, v194, v195
	v_cvt_pk_bf16_f32 v171, v192, v193
	v_lshl_add_u64 v[172:173], v[172:173], 1, v[182:183]
	global_store_dwordx4 v[172:173], v[168:171], off
	s_nop 1
	v_cvt_pk_bf16_f32 v168, v198, v199
	v_cvt_pk_bf16_f32 v169, v196, v197
	v_cvt_pk_bf16_f32 v170, v200, v201
	v_cvt_pk_bf16_f32 v171, v188, v189
	global_store_dwordx4 v[172:173], v[168:171], off offset:16
	v_mov_b32_e32 v172, v123
	v_mov_b32_e32 v173, v119
	v_mov_b32_e32 v170, v95
	v_mov_b32_e32 v171, v91
	v_mov_b32_e32 v168, v94
	v_mov_b32_e32 v169, v90
	v_pk_mul_f32 v[170:171], v[170:171], v[170:171]
	v_pk_mul_f32 v[172:173], v[172:173], v[172:173]
	v_pk_fma_f32 v[168:169], v[168:169], v[168:169], v[170:171]
	v_mov_b32_e32 v170, v96
	v_mov_b32_e32 v171, v92
	v_pk_fma_f32 v[168:169], v[170:171], v[170:171], v[168:169]
	v_mov_b32_e32 v170, v97
	v_mov_b32_e32 v171, v93
	v_pk_fma_f32 v[168:169], v[170:171], v[170:171], v[168:169]
	v_mov_b32_e32 v170, v122
	v_mov_b32_e32 v171, v118
	v_pk_fma_f32 v[170:171], v[170:171], v[170:171], v[172:173]
	v_mov_b32_e32 v172, v124
	v_mov_b32_e32 v173, v120
	v_pk_fma_f32 v[170:171], v[172:173], v[172:173], v[170:171]
	v_mov_b32_e32 v172, v125
	v_mov_b32_e32 v173, v121
	v_pk_fma_f32 v[170:171], v[172:173], v[172:173], v[170:171]
	v_add_f32_e32 v130, v168, v169
	v_add_f32_e32 v130, v130, v170
	v_add_f32_e32 v130, v130, v171
	ds_bpermute_b32 v167, v165, v130
	v_add_u32_e32 v168, s59, v250
	v_ashrrev_i32_e32 v169, 31, v168
	v_lshlrev_b64 v[168:169], 5, v[168:169]
	v_or_b32_e32 v168, v168, v158
	s_waitcnt lgkmcnt(0)
	v_add_f32_e32 v130, v130, v167
	ds_bpermute_b32 v167, v163, v130
	v_lshl_add_u64 v[190:191], v[168:169], 3, s[14:15]
	s_waitcnt lgkmcnt(0)
	v_add_f32_e32 v130, v130, v167
	v_fmamk_f32 v130, v130, 0x36800000, v176
	v_cmp_gt_f32_e32 vcc, s25, v130
	v_mul_f32_e32 v167, 0x4b800000, v130
	s_nop 0
	v_cndmask_b32_e32 v130, v130, v167, vcc
	v_rsq_f32_e32 v130, v130
	s_nop 0
	v_mul_f32_e32 v167, 0x45800000, v130
	v_cndmask_b32_e32 v130, v130, v167, vcc
	v_mul_f32_e32 v188, 0x3c800000, v130
	v_pk_mul_f32 v[170:171], v[94:95], v[188:189] op_sel_hi:[1,0]
	v_pk_mul_f32 v[172:173], v[96:97], v[188:189] op_sel_hi:[1,0]
	v_pk_mul_f32 v[184:185], v[14:15], v[170:171]
	v_pk_mul_f32 v[186:187], v[16:17], v[172:173]
	s_and_b64 vcc, exec, s[6:7]
	s_cbranch_vccnz .LBB0_497
	global_load_dwordx4 v[218:221], v[190:191], off
	global_load_dwordx4 v[222:225], v[190:191], off offset:16
	global_load_dwordx4 v[226:229], v[190:191], off offset:32
	global_load_dwordx4 v[230:233], v[190:191], off offset:48
	s_waitcnt vmcnt(3)
	v_mov_b64_e32 v[168:169], v[218:219]
	v_mov_b64_e32 v[170:171], v[220:221]
	v_pk_mul_f32 v[174:175], v[184:185], v[168:169] op_sel:[1,1] op_sel_hi:[1,0]
	v_mul_f32_e32 v130, v187, v171
	v_pk_mul_f32 v[172:173], v[184:185], v[168:169]
	v_pk_fma_f32 v[184:185], v[184:185], v[168:169], v[174:175] op_sel_hi:[0,1,1]
	v_pk_fma_f32 v[168:169], v[186:187], v[170:171], v[130:131] op_sel_hi:[1,1,0] neg_lo:[0,0,1] neg_hi:[0,0,1]
	v_mul_f32_e32 v130, v187, v170
	v_pk_fma_f32 v[170:171], v[186:187], v[170:171], v[130:131] op_sel:[0,1,0] op_sel_hi:[1,0,0]
	v_sub_f32_e32 v184, v172, v174
	v_mov_b32_e32 v186, v168
	v_mov_b32_e32 v187, v170
.LBB0_497:
	v_mov_b32_e32 v189, v188
	v_mov_b32_e32 v196, v188
	v_mov_b32_e32 v197, v188
	v_pk_mul_f32 v[168:169], v[92:93], v[196:197]
	v_pk_mul_f32 v[170:171], v[90:91], v[188:189]
	v_pk_mul_f32 v[192:193], v[12:13], v[168:169]
	s_and_b64 vcc, exec, s[6:7]
	v_pk_mul_f32 v[194:195], v[10:11], v[170:171]
	s_cbranch_vccnz .LBB0_499
	s_waitcnt vmcnt(2)
	v_mov_b64_e32 v[168:169], v[222:223]
	v_mov_b64_e32 v[170:171], v[224:225]
	v_pk_mul_f32 v[174:175], v[194:195], v[168:169] op_sel:[1,1] op_sel_hi:[1,0]
	v_mul_f32_e32 v130, v193, v171
	v_pk_mul_f32 v[172:173], v[194:195], v[168:169]
	v_pk_fma_f32 v[194:195], v[194:195], v[168:169], v[174:175] op_sel_hi:[0,1,1]
	v_pk_fma_f32 v[168:169], v[192:193], v[170:171], v[130:131] op_sel_hi:[1,1,0] neg_lo:[0,0,1] neg_hi:[0,0,1]
	v_mul_f32_e32 v130, v193, v170
	v_pk_fma_f32 v[170:171], v[192:193], v[170:171], v[130:131] op_sel:[0,1,0] op_sel_hi:[1,0,0]
	v_sub_f32_e32 v194, v172, v174
	v_mov_b32_e32 v192, v168
	v_mov_b32_e32 v193, v170
.LBB0_499:
	v_pk_mul_f32 v[168:169], v[124:125], v[196:197]
	v_pk_mul_f32 v[170:171], v[122:123], v[188:189]
	v_pk_mul_f32 v[196:197], v[8:9], v[168:169]
	s_and_b64 vcc, exec, s[6:7]
	v_pk_mul_f32 v[198:199], v[6:7], v[170:171]
	s_cbranch_vccnz .LBB0_501
	s_waitcnt vmcnt(1)
	v_mov_b64_e32 v[168:169], v[226:227]
	v_mov_b64_e32 v[170:171], v[228:229]
	v_pk_mul_f32 v[174:175], v[198:199], v[168:169] op_sel:[1,1] op_sel_hi:[1,0]
	v_mul_f32_e32 v130, v197, v171
	v_pk_mul_f32 v[172:173], v[198:199], v[168:169]
	v_pk_fma_f32 v[198:199], v[198:199], v[168:169], v[174:175] op_sel_hi:[0,1,1]
	v_pk_fma_f32 v[168:169], v[196:197], v[170:171], v[130:131] op_sel_hi:[1,1,0] neg_lo:[0,0,1] neg_hi:[0,0,1]
	v_mul_f32_e32 v130, v197, v170
	v_pk_fma_f32 v[170:171], v[196:197], v[170:171], v[130:131] op_sel:[0,1,0] op_sel_hi:[1,0,0]
	v_sub_f32_e32 v198, v172, v174
	v_mov_b32_e32 v196, v168
	v_mov_b32_e32 v197, v170
.LBB0_501:
	v_mov_b32_e32 v168, v188
	v_mov_b32_e32 v169, v188
	v_pk_mul_f32 v[168:169], v[120:121], v[168:169]
	v_pk_mul_f32 v[170:171], v[118:119], v[188:189]
	v_pk_mul_f32 v[188:189], v[4:5], v[168:169]
	s_and_b64 vcc, exec, s[6:7]
	v_pk_mul_f32 v[200:201], v[2:3], v[170:171]
	s_cbranch_vccnz .LBB0_503
	s_waitcnt vmcnt(0)
	v_mov_b64_e32 v[168:169], v[230:231]
	v_mov_b64_e32 v[170:171], v[232:233]
	v_pk_mul_f32 v[174:175], v[200:201], v[168:169] op_sel:[1,1] op_sel_hi:[1,0]
	v_mul_f32_e32 v130, v189, v171
	v_pk_mul_f32 v[172:173], v[200:201], v[168:169]
	v_pk_fma_f32 v[200:201], v[200:201], v[168:169], v[174:175] op_sel_hi:[0,1,1]
	v_pk_fma_f32 v[168:169], v[188:189], v[170:171], v[130:131] op_sel_hi:[1,1,0] neg_lo:[0,0,1] neg_hi:[0,0,1]
	v_mul_f32_e32 v130, v189, v170
	v_pk_fma_f32 v[170:171], v[188:189], v[170:171], v[130:131] op_sel:[0,1,0] op_sel_hi:[1,0,0]
	v_sub_f32_e32 v200, v172, v174
	v_mov_b32_e32 v188, v168
	v_mov_b32_e32 v189, v170
.LBB0_503:
	v_mad_i64_i32 v[172:173], s[60:61], s76, v250, 0
	v_cvt_pk_bf16_f32 v168, v184, v185
	v_cvt_pk_bf16_f32 v169, v186, v187
	v_cvt_pk_bf16_f32 v170, v194, v195
	v_cvt_pk_bf16_f32 v171, v192, v193
	v_lshl_add_u64 v[172:173], v[172:173], 1, v[182:183]
	global_store_dwordx4 v[172:173], v[168:171], off
	s_nop 1
	v_cvt_pk_bf16_f32 v168, v198, v199
	v_cvt_pk_bf16_f32 v169, v196, v197
	v_cvt_pk_bf16_f32 v170, v200, v201
	v_cvt_pk_bf16_f32 v171, v188, v189
	global_store_dwordx4 v[172:173], v[168:171], off offset:16
	v_mov_b32_e32 v172, v87
	v_mov_b32_e32 v173, v83
	v_mov_b32_e32 v170, v63
	v_mov_b32_e32 v171, v59
	v_mov_b32_e32 v168, v62
	v_mov_b32_e32 v169, v58
	v_pk_mul_f32 v[170:171], v[170:171], v[170:171]
	v_pk_mul_f32 v[172:173], v[172:173], v[172:173]
	v_pk_fma_f32 v[168:169], v[168:169], v[168:169], v[170:171]
	v_mov_b32_e32 v170, v64
	v_mov_b32_e32 v171, v60
	v_pk_fma_f32 v[168:169], v[170:171], v[170:171], v[168:169]
	v_mov_b32_e32 v170, v65
	v_mov_b32_e32 v171, v61
	v_pk_fma_f32 v[168:169], v[170:171], v[170:171], v[168:169]
	v_mov_b32_e32 v170, v86
	v_mov_b32_e32 v171, v82
	v_pk_fma_f32 v[170:171], v[170:171], v[170:171], v[172:173]
	v_mov_b32_e32 v172, v88
	v_mov_b32_e32 v173, v84
	v_pk_fma_f32 v[170:171], v[172:173], v[172:173], v[170:171]
	v_mov_b32_e32 v172, v89
	v_mov_b32_e32 v173, v85
	v_pk_fma_f32 v[170:171], v[172:173], v[172:173], v[170:171]
	v_add_f32_e32 v130, v168, v169
	v_add_f32_e32 v130, v130, v170
	v_add_f32_e32 v130, v130, v171
	ds_bpermute_b32 v167, v165, v130
	v_add_u32_e32 v168, s59, v252
	v_ashrrev_i32_e32 v169, 31, v168
	v_lshlrev_b64 v[168:169], 5, v[168:169]
	v_or_b32_e32 v168, v168, v158
	s_waitcnt lgkmcnt(0)
	v_add_f32_e32 v130, v130, v167
	ds_bpermute_b32 v167, v163, v130
	v_lshl_add_u64 v[190:191], v[168:169], 3, s[14:15]
	s_waitcnt lgkmcnt(0)
	v_add_f32_e32 v130, v130, v167
	v_fmamk_f32 v130, v130, 0x36800000, v176
	v_cmp_gt_f32_e32 vcc, s25, v130
	v_mul_f32_e32 v167, 0x4b800000, v130
	s_nop 0
	v_cndmask_b32_e32 v130, v130, v167, vcc
	v_rsq_f32_e32 v130, v130
	s_nop 0
	v_mul_f32_e32 v167, 0x45800000, v130
	v_cndmask_b32_e32 v130, v130, v167, vcc
	v_mul_f32_e32 v188, 0x3c800000, v130
	v_pk_mul_f32 v[170:171], v[62:63], v[188:189] op_sel_hi:[1,0]
	v_pk_mul_f32 v[172:173], v[64:65], v[188:189] op_sel_hi:[1,0]
	v_pk_mul_f32 v[184:185], v[14:15], v[170:171]
	v_pk_mul_f32 v[186:187], v[16:17], v[172:173]
	s_and_b64 vcc, exec, s[6:7]
	s_cbranch_vccnz .LBB0_505
	global_load_dwordx4 v[218:221], v[190:191], off
	global_load_dwordx4 v[222:225], v[190:191], off offset:16
	global_load_dwordx4 v[226:229], v[190:191], off offset:32
	global_load_dwordx4 v[230:233], v[190:191], off offset:48
	s_waitcnt vmcnt(3)
	v_mov_b64_e32 v[168:169], v[218:219]
	v_mov_b64_e32 v[170:171], v[220:221]
	v_pk_mul_f32 v[174:175], v[184:185], v[168:169] op_sel:[1,1] op_sel_hi:[1,0]
	v_mul_f32_e32 v130, v187, v171
	v_pk_mul_f32 v[172:173], v[184:185], v[168:169]
	v_pk_fma_f32 v[184:185], v[184:185], v[168:169], v[174:175] op_sel_hi:[0,1,1]
	v_pk_fma_f32 v[168:169], v[186:187], v[170:171], v[130:131] op_sel_hi:[1,1,0] neg_lo:[0,0,1] neg_hi:[0,0,1]
	v_mul_f32_e32 v130, v187, v170
	v_pk_fma_f32 v[170:171], v[186:187], v[170:171], v[130:131] op_sel:[0,1,0] op_sel_hi:[1,0,0]
	v_sub_f32_e32 v184, v172, v174
	v_mov_b32_e32 v186, v168
	v_mov_b32_e32 v187, v170
.LBB0_505:
	v_mov_b32_e32 v189, v188
	v_mov_b32_e32 v196, v188
	v_mov_b32_e32 v197, v188
	v_pk_mul_f32 v[168:169], v[60:61], v[196:197]
	v_pk_mul_f32 v[170:171], v[58:59], v[188:189]
	v_pk_mul_f32 v[192:193], v[12:13], v[168:169]
	s_and_b64 vcc, exec, s[6:7]
	v_pk_mul_f32 v[194:195], v[10:11], v[170:171]
	s_cbranch_vccnz .LBB0_507
	s_waitcnt vmcnt(2)
	v_mov_b64_e32 v[168:169], v[222:223]
	v_mov_b64_e32 v[170:171], v[224:225]
	v_pk_mul_f32 v[174:175], v[194:195], v[168:169] op_sel:[1,1] op_sel_hi:[1,0]
	v_mul_f32_e32 v130, v193, v171
	v_pk_mul_f32 v[172:173], v[194:195], v[168:169]
	v_pk_fma_f32 v[194:195], v[194:195], v[168:169], v[174:175] op_sel_hi:[0,1,1]
	v_pk_fma_f32 v[168:169], v[192:193], v[170:171], v[130:131] op_sel_hi:[1,1,0] neg_lo:[0,0,1] neg_hi:[0,0,1]
	v_mul_f32_e32 v130, v193, v170
	v_pk_fma_f32 v[170:171], v[192:193], v[170:171], v[130:131] op_sel:[0,1,0] op_sel_hi:[1,0,0]
	v_sub_f32_e32 v194, v172, v174
	v_mov_b32_e32 v192, v168
	v_mov_b32_e32 v193, v170
.LBB0_507:
	v_pk_mul_f32 v[168:169], v[88:89], v[196:197]
	v_pk_mul_f32 v[170:171], v[86:87], v[188:189]
	v_pk_mul_f32 v[196:197], v[8:9], v[168:169]
	s_and_b64 vcc, exec, s[6:7]
	v_pk_mul_f32 v[198:199], v[6:7], v[170:171]
	s_cbranch_vccnz .LBB0_509
	s_waitcnt vmcnt(1)
	v_mov_b64_e32 v[168:169], v[226:227]
	v_mov_b64_e32 v[170:171], v[228:229]
	v_pk_mul_f32 v[174:175], v[198:199], v[168:169] op_sel:[1,1] op_sel_hi:[1,0]
	v_mul_f32_e32 v130, v197, v171
	v_pk_mul_f32 v[172:173], v[198:199], v[168:169]
	v_pk_fma_f32 v[198:199], v[198:199], v[168:169], v[174:175] op_sel_hi:[0,1,1]
	v_pk_fma_f32 v[168:169], v[196:197], v[170:171], v[130:131] op_sel_hi:[1,1,0] neg_lo:[0,0,1] neg_hi:[0,0,1]
	v_mul_f32_e32 v130, v197, v170
	v_pk_fma_f32 v[170:171], v[196:197], v[170:171], v[130:131] op_sel:[0,1,0] op_sel_hi:[1,0,0]
	v_sub_f32_e32 v198, v172, v174
	v_mov_b32_e32 v196, v168
	v_mov_b32_e32 v197, v170
.LBB0_509:
	v_mov_b32_e32 v168, v188
	v_mov_b32_e32 v169, v188
	v_pk_mul_f32 v[168:169], v[84:85], v[168:169]
	v_pk_mul_f32 v[170:171], v[82:83], v[188:189]
	v_pk_mul_f32 v[188:189], v[4:5], v[168:169]
	s_and_b64 vcc, exec, s[6:7]
	v_pk_mul_f32 v[200:201], v[2:3], v[170:171]
	s_cbranch_vccnz .LBB0_511
	s_waitcnt vmcnt(0)
	v_mov_b64_e32 v[168:169], v[230:231]
	v_mov_b64_e32 v[170:171], v[232:233]
	v_pk_mul_f32 v[174:175], v[200:201], v[168:169] op_sel:[1,1] op_sel_hi:[1,0]
	v_mul_f32_e32 v130, v189, v171
	v_pk_mul_f32 v[172:173], v[200:201], v[168:169]
	v_pk_fma_f32 v[200:201], v[200:201], v[168:169], v[174:175] op_sel_hi:[0,1,1]
	v_pk_fma_f32 v[168:169], v[188:189], v[170:171], v[130:131] op_sel_hi:[1,1,0] neg_lo:[0,0,1] neg_hi:[0,0,1]
	v_mul_f32_e32 v130, v189, v170
	v_pk_fma_f32 v[170:171], v[188:189], v[170:171], v[130:131] op_sel:[0,1,0] op_sel_hi:[1,0,0]
	v_sub_f32_e32 v200, v172, v174
	v_mov_b32_e32 v188, v168
	v_mov_b32_e32 v189, v170
.LBB0_511:
	v_mad_i64_i32 v[172:173], s[60:61], s76, v252, 0
	v_cvt_pk_bf16_f32 v168, v184, v185
	v_cvt_pk_bf16_f32 v169, v186, v187
	v_cvt_pk_bf16_f32 v170, v194, v195
	v_cvt_pk_bf16_f32 v171, v192, v193
	v_lshl_add_u64 v[172:173], v[172:173], 1, v[182:183]
	global_store_dwordx4 v[172:173], v[168:171], off
	s_nop 1
	v_cvt_pk_bf16_f32 v168, v198, v199
	v_cvt_pk_bf16_f32 v169, v196, v197
	v_cvt_pk_bf16_f32 v170, v200, v201
	v_cvt_pk_bf16_f32 v171, v188, v189
	global_store_dwordx4 v[172:173], v[168:171], off offset:16
	v_mov_b32_e32 v172, v55
	v_mov_b32_e32 v173, v47
	v_mov_b32_e32 v170, v39
	v_mov_b32_e32 v171, v35
	v_mov_b32_e32 v168, v38
	v_mov_b32_e32 v169, v34
	v_pk_mul_f32 v[170:171], v[170:171], v[170:171]
	v_pk_mul_f32 v[172:173], v[172:173], v[172:173]
	v_pk_fma_f32 v[168:169], v[168:169], v[168:169], v[170:171]
	v_mov_b32_e32 v170, v40
	v_mov_b32_e32 v171, v36
	v_pk_fma_f32 v[168:169], v[170:171], v[170:171], v[168:169]
	v_mov_b32_e32 v170, v41
	v_mov_b32_e32 v171, v37
	v_pk_fma_f32 v[168:169], v[170:171], v[170:171], v[168:169]
	v_mov_b32_e32 v170, v54
	v_mov_b32_e32 v171, v46
	v_pk_fma_f32 v[170:171], v[170:171], v[170:171], v[172:173]
	v_mov_b32_e32 v172, v56
	v_mov_b32_e32 v173, v48
	v_pk_fma_f32 v[170:171], v[172:173], v[172:173], v[170:171]
	v_mov_b32_e32 v172, v57
	v_mov_b32_e32 v173, v49
	v_pk_fma_f32 v[170:171], v[172:173], v[172:173], v[170:171]
	v_add_f32_e32 v130, v168, v169
	v_add_f32_e32 v130, v130, v170
	v_add_f32_e32 v130, v130, v171
	ds_bpermute_b32 v167, v165, v130
	v_add_u32_e32 v168, s59, v202
	v_ashrrev_i32_e32 v169, 31, v168
	v_lshlrev_b64 v[168:169], 5, v[168:169]
	v_or_b32_e32 v168, v168, v158
	s_waitcnt lgkmcnt(0)
	v_add_f32_e32 v130, v130, v167
	ds_bpermute_b32 v167, v163, v130
	v_lshl_add_u64 v[190:191], v[168:169], 3, s[14:15]
	s_waitcnt lgkmcnt(0)
	v_add_f32_e32 v130, v130, v167
	v_fmamk_f32 v130, v130, 0x36800000, v176
	v_cmp_gt_f32_e32 vcc, s25, v130
	v_mul_f32_e32 v167, 0x4b800000, v130
	s_nop 0
	v_cndmask_b32_e32 v130, v130, v167, vcc
	v_rsq_f32_e32 v130, v130
	s_nop 0
	v_mul_f32_e32 v167, 0x45800000, v130
	v_cndmask_b32_e32 v130, v130, v167, vcc
	v_mul_f32_e32 v188, 0x3c800000, v130
	v_pk_mul_f32 v[170:171], v[38:39], v[188:189] op_sel_hi:[1,0]
	v_pk_mul_f32 v[172:173], v[40:41], v[188:189] op_sel_hi:[1,0]
	v_pk_mul_f32 v[184:185], v[14:15], v[170:171]
	v_pk_mul_f32 v[186:187], v[16:17], v[172:173]
	s_and_b64 vcc, exec, s[6:7]
	s_cbranch_vccnz .LBB0_513
	global_load_dwordx4 v[218:221], v[190:191], off
	global_load_dwordx4 v[222:225], v[190:191], off offset:16
	global_load_dwordx4 v[226:229], v[190:191], off offset:32
	global_load_dwordx4 v[230:233], v[190:191], off offset:48
	s_waitcnt vmcnt(3)
	v_mov_b64_e32 v[168:169], v[218:219]
	v_mov_b64_e32 v[170:171], v[220:221]
	v_pk_mul_f32 v[174:175], v[184:185], v[168:169] op_sel:[1,1] op_sel_hi:[1,0]
	v_mul_f32_e32 v130, v187, v171
	v_pk_mul_f32 v[172:173], v[184:185], v[168:169]
	v_pk_fma_f32 v[184:185], v[184:185], v[168:169], v[174:175] op_sel_hi:[0,1,1]
	v_pk_fma_f32 v[168:169], v[186:187], v[170:171], v[130:131] op_sel_hi:[1,1,0] neg_lo:[0,0,1] neg_hi:[0,0,1]
	v_mul_f32_e32 v130, v187, v170
	v_pk_fma_f32 v[170:171], v[186:187], v[170:171], v[130:131] op_sel:[0,1,0] op_sel_hi:[1,0,0]
	v_sub_f32_e32 v184, v172, v174
	v_mov_b32_e32 v186, v168
	v_mov_b32_e32 v187, v170
.LBB0_513:
	v_mov_b32_e32 v189, v188
	v_mov_b32_e32 v196, v188
	v_mov_b32_e32 v197, v188
	v_pk_mul_f32 v[168:169], v[36:37], v[196:197]
	v_pk_mul_f32 v[170:171], v[34:35], v[188:189]
	v_pk_mul_f32 v[192:193], v[12:13], v[168:169]
	s_and_b64 vcc, exec, s[6:7]
	v_pk_mul_f32 v[194:195], v[10:11], v[170:171]
	s_cbranch_vccnz .LBB0_515
	s_waitcnt vmcnt(2)
	v_mov_b64_e32 v[168:169], v[222:223]
	v_mov_b64_e32 v[170:171], v[224:225]
	v_pk_mul_f32 v[174:175], v[194:195], v[168:169] op_sel:[1,1] op_sel_hi:[1,0]
	v_mul_f32_e32 v130, v193, v171
	v_pk_mul_f32 v[172:173], v[194:195], v[168:169]
	v_pk_fma_f32 v[194:195], v[194:195], v[168:169], v[174:175] op_sel_hi:[0,1,1]
	v_pk_fma_f32 v[168:169], v[192:193], v[170:171], v[130:131] op_sel_hi:[1,1,0] neg_lo:[0,0,1] neg_hi:[0,0,1]
	v_mul_f32_e32 v130, v193, v170
	v_pk_fma_f32 v[170:171], v[192:193], v[170:171], v[130:131] op_sel:[0,1,0] op_sel_hi:[1,0,0]
	v_sub_f32_e32 v194, v172, v174
	v_mov_b32_e32 v192, v168
	v_mov_b32_e32 v193, v170
.LBB0_515:
	v_pk_mul_f32 v[168:169], v[56:57], v[196:197]
	v_pk_mul_f32 v[170:171], v[54:55], v[188:189]
	v_pk_mul_f32 v[196:197], v[8:9], v[168:169]
	s_and_b64 vcc, exec, s[6:7]
	v_pk_mul_f32 v[198:199], v[6:7], v[170:171]
	s_cbranch_vccnz .LBB0_517
	s_waitcnt vmcnt(1)
	v_mov_b64_e32 v[168:169], v[226:227]
	v_mov_b64_e32 v[170:171], v[228:229]
	v_pk_mul_f32 v[174:175], v[198:199], v[168:169] op_sel:[1,1] op_sel_hi:[1,0]
	v_mul_f32_e32 v130, v197, v171
	v_pk_mul_f32 v[172:173], v[198:199], v[168:169]
	v_pk_fma_f32 v[198:199], v[198:199], v[168:169], v[174:175] op_sel_hi:[0,1,1]
	v_pk_fma_f32 v[168:169], v[196:197], v[170:171], v[130:131] op_sel_hi:[1,1,0] neg_lo:[0,0,1] neg_hi:[0,0,1]
	v_mul_f32_e32 v130, v197, v170
	v_pk_fma_f32 v[170:171], v[196:197], v[170:171], v[130:131] op_sel:[0,1,0] op_sel_hi:[1,0,0]
	v_sub_f32_e32 v198, v172, v174
	v_mov_b32_e32 v196, v168
	v_mov_b32_e32 v197, v170
.LBB0_517:
	v_mov_b32_e32 v168, v188
	v_mov_b32_e32 v169, v188
	v_pk_mul_f32 v[168:169], v[48:49], v[168:169]
	v_pk_mul_f32 v[170:171], v[46:47], v[188:189]
	v_pk_mul_f32 v[188:189], v[4:5], v[168:169]
	s_and_b64 vcc, exec, s[6:7]
	v_pk_mul_f32 v[200:201], v[2:3], v[170:171]
	s_cbranch_vccnz .LBB0_519
	s_waitcnt vmcnt(0)
	v_mov_b64_e32 v[168:169], v[230:231]
	v_mov_b64_e32 v[170:171], v[232:233]
	v_pk_mul_f32 v[174:175], v[200:201], v[168:169] op_sel:[1,1] op_sel_hi:[1,0]
	v_mul_f32_e32 v130, v189, v171
	v_pk_mul_f32 v[172:173], v[200:201], v[168:169]
	v_pk_fma_f32 v[200:201], v[200:201], v[168:169], v[174:175] op_sel_hi:[0,1,1]
	v_pk_fma_f32 v[168:169], v[188:189], v[170:171], v[130:131] op_sel_hi:[1,1,0] neg_lo:[0,0,1] neg_hi:[0,0,1]
	v_mul_f32_e32 v130, v189, v170
	v_pk_fma_f32 v[170:171], v[188:189], v[170:171], v[130:131] op_sel:[0,1,0] op_sel_hi:[1,0,0]
	v_sub_f32_e32 v200, v172, v174
	v_mov_b32_e32 v188, v168
	v_mov_b32_e32 v189, v170
.LBB0_519:
	v_mad_i64_i32 v[172:173], s[60:61], s76, v202, 0
	v_cvt_pk_bf16_f32 v168, v184, v185
	v_cvt_pk_bf16_f32 v169, v186, v187
	v_cvt_pk_bf16_f32 v170, v194, v195
	v_cvt_pk_bf16_f32 v171, v192, v193
	v_lshl_add_u64 v[172:173], v[172:173], 1, v[182:183]
	global_store_dwordx4 v[172:173], v[168:171], off
	s_nop 1
	v_cvt_pk_bf16_f32 v168, v198, v199
	v_cvt_pk_bf16_f32 v169, v196, v197
	v_cvt_pk_bf16_f32 v170, v200, v201
	v_cvt_pk_bf16_f32 v171, v188, v189
	global_store_dwordx4 v[172:173], v[168:171], off offset:16
	v_mov_b32_e32 v172, v31
	v_mov_b32_e32 v173, v27
	v_mov_b32_e32 v170, v23
	v_mov_b32_e32 v171, v19
	v_mov_b32_e32 v168, v22
	v_mov_b32_e32 v169, v18
	v_pk_mul_f32 v[170:171], v[170:171], v[170:171]
	v_pk_mul_f32 v[172:173], v[172:173], v[172:173]
	v_pk_fma_f32 v[168:169], v[168:169], v[168:169], v[170:171]
	v_mov_b32_e32 v170, v24
	v_mov_b32_e32 v171, v20
	v_pk_fma_f32 v[168:169], v[170:171], v[170:171], v[168:169]
	v_mov_b32_e32 v170, v25
	v_mov_b32_e32 v171, v21
	v_pk_fma_f32 v[168:169], v[170:171], v[170:171], v[168:169]
	v_mov_b32_e32 v170, v30
	v_mov_b32_e32 v171, v26
	v_pk_fma_f32 v[170:171], v[170:171], v[170:171], v[172:173]
	v_mov_b32_e32 v172, v32
	v_mov_b32_e32 v173, v28
	v_pk_fma_f32 v[170:171], v[172:173], v[172:173], v[170:171]
	v_mov_b32_e32 v172, v33
	v_mov_b32_e32 v173, v29
	v_pk_fma_f32 v[170:171], v[172:173], v[172:173], v[170:171]
	v_add_f32_e32 v130, v168, v169
	v_add_f32_e32 v130, v130, v170
	v_add_f32_e32 v130, v130, v171
	ds_bpermute_b32 v165, v165, v130
	v_add_u32_e32 v168, s59, v210
	v_ashrrev_i32_e32 v169, 31, v168
	v_lshlrev_b64 v[168:169], 5, v[168:169]
	v_or_b32_e32 v168, v168, v158
	s_waitcnt lgkmcnt(0)
	v_add_f32_e32 v130, v130, v165
	ds_bpermute_b32 v163, v163, v130
	v_lshl_add_u64 v[186:187], v[168:169], 3, s[14:15]
	s_waitcnt lgkmcnt(0)
	v_add_f32_e32 v130, v130, v163
	v_fmamk_f32 v130, v130, 0x36800000, v176
	v_cmp_gt_f32_e32 vcc, s25, v130
	v_mul_f32_e32 v163, 0x4b800000, v130
	s_nop 0
	v_cndmask_b32_e32 v130, v130, v163, vcc
	v_rsq_f32_e32 v130, v130
	s_nop 0
	v_mul_f32_e32 v163, 0x45800000, v130
	v_cndmask_b32_e32 v130, v130, v163, vcc
	v_mul_f32_e32 v184, 0x3c800000, v130
	v_pk_mul_f32 v[170:171], v[22:23], v[184:185] op_sel_hi:[1,0]
	v_pk_mul_f32 v[172:173], v[24:25], v[184:185] op_sel_hi:[1,0]
	v_pk_mul_f32 v[14:15], v[14:15], v[170:171]
	v_pk_mul_f32 v[16:17], v[16:17], v[172:173]
	s_and_b64 vcc, exec, s[6:7]
	s_cbranch_vccnz .LBB0_521
	global_load_dwordx4 v[218:221], v[186:187], off
	global_load_dwordx4 v[222:225], v[186:187], off offset:16
	global_load_dwordx4 v[226:229], v[186:187], off offset:32
	global_load_dwordx4 v[230:233], v[186:187], off offset:48
	s_waitcnt vmcnt(3)
	v_mov_b64_e32 v[168:169], v[218:219]
	v_mov_b64_e32 v[170:171], v[220:221]
	v_pk_mul_f32 v[174:175], v[14:15], v[168:169] op_sel:[1,1] op_sel_hi:[1,0]
	v_pk_mul_f32 v[172:173], v[14:15], v[168:169]
	v_pk_fma_f32 v[14:15], v[14:15], v[168:169], v[174:175] op_sel_hi:[0,1,1]
	v_mul_f32_e32 v14, v17, v171
	v_pk_fma_f32 v[168:169], v[16:17], v[170:171], v[14:15] op_sel_hi:[1,1,0] neg_lo:[0,0,1] neg_hi:[0,0,1]
	v_mul_f32_e32 v14, v17, v170
	v_pk_fma_f32 v[170:171], v[16:17], v[170:171], v[14:15] op_sel:[0,1,0] op_sel_hi:[1,0,0]
	v_sub_f32_e32 v14, v172, v174
	v_mov_b32_e32 v16, v168
	v_mov_b32_e32 v17, v170
.LBB0_521:
	v_mov_b32_e32 v185, v184
	v_mov_b32_e32 v188, v184
	v_mov_b32_e32 v189, v184
	v_pk_mul_f32 v[168:169], v[20:21], v[188:189]
	v_pk_mul_f32 v[170:171], v[18:19], v[184:185]
	v_pk_mul_f32 v[12:13], v[12:13], v[168:169]
	s_and_b64 vcc, exec, s[6:7]
	v_pk_mul_f32 v[10:11], v[10:11], v[170:171]
	s_cbranch_vccnz .LBB0_523
	s_waitcnt vmcnt(2)
	v_mov_b64_e32 v[168:169], v[222:223]
	v_mov_b64_e32 v[170:171], v[224:225]
	v_pk_mul_f32 v[174:175], v[10:11], v[168:169] op_sel:[1,1] op_sel_hi:[1,0]
	v_pk_mul_f32 v[172:173], v[10:11], v[168:169]
	v_pk_fma_f32 v[10:11], v[10:11], v[168:169], v[174:175] op_sel_hi:[0,1,1]
	v_mul_f32_e32 v10, v13, v171
	v_pk_fma_f32 v[168:169], v[12:13], v[170:171], v[10:11] op_sel_hi:[1,1,0] neg_lo:[0,0,1] neg_hi:[0,0,1]
	v_mul_f32_e32 v10, v13, v170
	v_pk_fma_f32 v[170:171], v[12:13], v[170:171], v[10:11] op_sel:[0,1,0] op_sel_hi:[1,0,0]
	v_sub_f32_e32 v10, v172, v174
	v_mov_b32_e32 v12, v168
	v_mov_b32_e32 v13, v170
.LBB0_523:
	v_pk_mul_f32 v[168:169], v[32:33], v[188:189]
	v_pk_mul_f32 v[170:171], v[30:31], v[184:185]
	v_pk_mul_f32 v[8:9], v[8:9], v[168:169]
	s_and_b64 vcc, exec, s[6:7]
	v_pk_mul_f32 v[6:7], v[6:7], v[170:171]
	s_cbranch_vccnz .LBB0_525
	s_waitcnt vmcnt(1)
	v_mov_b64_e32 v[168:169], v[226:227]
	v_mov_b64_e32 v[170:171], v[228:229]
	v_pk_mul_f32 v[174:175], v[6:7], v[168:169] op_sel:[1,1] op_sel_hi:[1,0]
	v_pk_mul_f32 v[172:173], v[6:7], v[168:169]
	v_pk_fma_f32 v[6:7], v[6:7], v[168:169], v[174:175] op_sel_hi:[0,1,1]
	v_mul_f32_e32 v6, v9, v171
	v_pk_fma_f32 v[168:169], v[8:9], v[170:171], v[6:7] op_sel_hi:[1,1,0] neg_lo:[0,0,1] neg_hi:[0,0,1]
	v_mul_f32_e32 v6, v9, v170
	v_pk_fma_f32 v[170:171], v[8:9], v[170:171], v[6:7] op_sel:[0,1,0] op_sel_hi:[1,0,0]
	v_sub_f32_e32 v6, v172, v174
	v_mov_b32_e32 v8, v168
	v_mov_b32_e32 v9, v170
.LBB0_525:
	v_mov_b32_e32 v168, v184
	v_mov_b32_e32 v169, v184
	v_pk_mul_f32 v[168:169], v[28:29], v[168:169]
	v_pk_mul_f32 v[170:171], v[26:27], v[184:185]
	v_pk_mul_f32 v[4:5], v[4:5], v[168:169]
	s_and_b64 vcc, exec, s[6:7]
	v_pk_mul_f32 v[2:3], v[2:3], v[170:171]
	s_cbranch_vccnz .LBB0_527
	s_waitcnt vmcnt(0)
	v_mov_b64_e32 v[168:169], v[230:231]
	v_mov_b64_e32 v[170:171], v[232:233]
	v_pk_mul_f32 v[174:175], v[2:3], v[168:169] op_sel:[1,1] op_sel_hi:[1,0]
	v_pk_mul_f32 v[172:173], v[2:3], v[168:169]
	v_pk_fma_f32 v[2:3], v[2:3], v[168:169], v[174:175] op_sel_hi:[0,1,1]
	v_mul_f32_e32 v2, v5, v171
	v_pk_fma_f32 v[168:169], v[4:5], v[170:171], v[2:3] op_sel_hi:[1,1,0] neg_lo:[0,0,1] neg_hi:[0,0,1]
	v_mul_f32_e32 v2, v5, v170
	v_pk_fma_f32 v[170:171], v[4:5], v[170:171], v[2:3] op_sel:[0,1,0] op_sel_hi:[1,0,0]
	v_sub_f32_e32 v2, v172, v174
	v_mov_b32_e32 v4, v168
	v_mov_b32_e32 v5, v170

.LBB0_608:
	s_or_b64 exec, exec, s[4:5]
	s_mov_b64 s[66:67], s[96:97]
	s_waitcnt lgkmcnt(0)
	s_barrier
	s_mov_b32 s100, 0
	s_load_dwordx2 s[68:69], s[66:67], 0xe0
	v_readlane_b32 s4, v254, 26
	v_readlane_b32 s5, v254, 27
	s_and_b64 s[4:5], s[4:5], exec
	s_movk_i32 s1, 0xa8
	s_cselect_b32 s65, s1, 0xdc
	s_lshl_b32 s22, s44, 9
	s_lshl_b64 s[4:5], s[22:23], 2
	s_waitcnt lgkmcnt(0)
	s_add_u32 s1, s68, s4
	s_addc_u32 s2, s69, s5
	s_add_u32 s70, s1, 0x8100
	s_addc_u32 s71, s2, 0
	s_lshl_b32 s22, s44, 5
	s_lshl_b64 s[4:5], s[22:23], 2
	s_add_u32 s1, s68, s4
	s_addc_u32 s2, s69, s5
	s_add_u32 s72, s1, 0xe000
	s_addc_u32 s73, s2, 0
	s_add_u32 s74, s68, 0x38028000
	s_addc_u32 s75, s69, 0
	s_add_u32 s1, s68, 0x3d868000
	v_writelane_b32 v254, s1, 32
	s_addc_u32 s1, s69, 0
	s_add_u32 s76, s68, 0x38038000
	s_addc_u32 s77, s69, 0
	s_add_u32 s4, s68, 0x38028080
	v_writelane_b32 v254, s1, 33
	s_addc_u32 s5, s69, 0
	v_writelane_b32 v254, s4, 34
	s_add_u32 s1, s68, 0x5c068000
	s_addc_u32 s79, s69, 0
	v_writelane_b32 v254, s5, 35
	v_writelane_b32 v254, s1, 36
	s_add_u32 s1, s68, 0x5e468000
	v_writelane_b32 v254, s1, 37
	s_mul_hi_u32 s1, s44, 0x2400
	s_addc_u32 s63, s69, 0
	v_writelane_b32 v254, s1, 12
	s_mul_i32 s1, s44, 0x2400
	s_add_u32 s78, s68, 0x5ed68000
	v_writelane_b32 v254, s1, 10
	s_mul_hi_u32 s1, s44, 0xc00
	s_addc_u32 s62, s69, 0
	s_lshl_b64 s[4:5], s[44:45], 19
	v_writelane_b32 v254, s1, 14
	s_mul_i32 s1, s44, 0xc00
	s_lshl_b64 s[80:81], s[44:45], 11
	v_writelane_b32 v254, s1, 5
	s_add_u32 s1, s68, 0x5bc68000
	v_writelane_b32 v254, s1, 38
	s_addc_u32 s1, s69, 0
	v_writelane_b32 v254, s1, 39
	s_add_u32 s1, s68, 0x37028000
	v_writelane_b32 v254, s1, 40
	s_addc_u32 s1, s69, 0
	s_mov_b64 s[6:7], s[44:45]
	s_add_u32 s45, s68, 0x3c868000
	s_addc_u32 s97, s69, 0
	s_lshl_b64 s[6:7], s[6:7], 22
	s_add_u32 s46, s68, 0x59c68000
	s_addc_u32 s47, s69, 0
	s_add_u32 s50, s68, 0x59668000
	s_addc_u32 s51, s69, 0
	v_writelane_b32 v254, s1, 41
	s_add_u32 s1, s68, s4
	s_addc_u32 s2, s69, s5
	s_add_u32 s1, s1, 0x36e28000
	v_writelane_b32 v254, s1, 42
	s_addc_u32 s1, s2, 0
	s_add_u32 s53, s68, 0x5ed68400
	s_addc_u32 s2, s69, 0
	s_add_u32 s58, s68, 0x56668000
	s_addc_u32 s59, s69, 0
	v_writelane_b32 v254, s1, 43
	s_add_u32 s1, s68, s6
	s_addc_u32 s4, s69, s7
	s_add_u32 s34, s1, 0x35e28000
	s_getreg_b32 s96, hwreg(HW_REG_XCC_ID, 0, 4)
	s_addc_u32 s35, s4, 0
	s_mov_b32 s36, 0
	s_branch .LBB0_610

.LBB0_639:
	s_and_b64 vcc, exec, s[4:5]
	s_cbranch_vccz .LBB0_666
	s_cmp_lg_u32 s100, 0
	s_cbranch_scc0 .Lnegc_calc_a
	v_mov_b32_e32 v50, v0
	s_nop 0
	v_readfirstlane_b32 s10, v50
	s_mov_b32 s11, s101
	s_ashr_i32 s1, s10, 6
	s_cmp_lt_i32 s1, 4
	s_branch .Lnegc_done_a
.Lnegc_calc_a:
	v_mov_b32_e32 v2, v0
	s_load_dwordx4 s[4:7], s[66:67], 0x48
	v_readlane_b32 s10, v254, 30
	v_and_b32_e32 v6, 64, v177
	v_add_u32_e32 v6, 64, v6
	v_and_or_b32 v130, v2, 63, s10
	v_lshlrev_b64 v[2:3], 2, v[130:131]
	s_waitcnt lgkmcnt(0)
	v_lshl_add_u64 v[4:5], s[4:5], 0, v[2:3]
	v_lshl_add_u64 v[2:3], s[6:7], 0, v[2:3]
	global_load_dword v2, v[2:3], off
	v_xor_b32_e32 v7, 32, v177
	global_load_dword v4, v[4:5], off
	v_cmp_lt_i32_e32 vcc, v7, v6
	v_mov_b32_e32 v50, v0
	v_readlane_b32 s11, v254, 31
	v_cndmask_b32_e32 v7, v177, v7, vcc
	v_lshlrev_b32_e32 v7, 2, v7
	v_readfirstlane_b32 s10, v50
	s_ashr_i32 s1, s10, 6
	s_cmp_lt_i32 s1, 4
	s_waitcnt vmcnt(0)
	v_and_b32_e32 v3, 0x7fffffff, v2
	ds_bpermute_b32 v3, v7, v3
	v_and_b32_e32 v5, 0x7fffffff, v4
	ds_bpermute_b32 v5, v7, v5
	v_max_f32_e64 v2, |v2|, |v2|
	v_max_f32_e64 v4, |v4|, |v4|
	s_waitcnt lgkmcnt(1)
	v_max_f32_e32 v3, v3, v3
	v_max_f32_e32 v2, v2, v3
	v_xor_b32_e32 v3, 16, v177
	v_cmp_lt_i32_e32 vcc, v3, v6
	s_waitcnt lgkmcnt(0)
	v_max_f32_e32 v5, v5, v5
	v_max_f32_e32 v4, v4, v5
	v_cndmask_b32_e32 v3, v177, v3, vcc
	v_lshlrev_b32_e32 v3, 2, v3
	ds_bpermute_b32 v5, v3, v4
	ds_bpermute_b32 v3, v3, v2
	s_waitcnt lgkmcnt(1)
	v_max_f32_e32 v5, v5, v5
	s_waitcnt lgkmcnt(0)
	v_max_f32_e32 v3, v3, v3
	v_max_f32_e32 v2, v2, v3
	v_xor_b32_e32 v3, 8, v177
	v_cmp_lt_i32_e32 vcc, v3, v6
	v_max_f32_e32 v4, v4, v5
	s_nop 0
	v_cndmask_b32_e32 v3, v177, v3, vcc
	v_lshlrev_b32_e32 v3, 2, v3
	ds_bpermute_b32 v5, v3, v4
	ds_bpermute_b32 v3, v3, v2
	s_waitcnt lgkmcnt(1)
	v_max_f32_e32 v5, v5, v5
	s_waitcnt lgkmcnt(0)
	v_max_f32_e32 v3, v3, v3
	v_max_f32_e32 v2, v2, v3
	v_xor_b32_e32 v3, 4, v177
	v_cmp_lt_i32_e32 vcc, v3, v6
	v_max_f32_e32 v4, v4, v5
	s_nop 0
	v_cndmask_b32_e32 v3, v177, v3, vcc
	v_lshlrev_b32_e32 v3, 2, v3
	ds_bpermute_b32 v5, v3, v4
	ds_bpermute_b32 v3, v3, v2
	s_waitcnt lgkmcnt(1)
	v_max_f32_e32 v5, v5, v5
	s_waitcnt lgkmcnt(0)
	v_max_f32_e32 v3, v3, v3
	v_max_f32_e32 v2, v2, v3
	v_xor_b32_e32 v3, 2, v177
	v_cmp_lt_i32_e32 vcc, v3, v6
	v_max_f32_e32 v4, v4, v5
	s_nop 0
	v_cndmask_b32_e32 v3, v177, v3, vcc
	v_lshlrev_b32_e32 v3, 2, v3
	ds_bpermute_b32 v5, v3, v4
	ds_bpermute_b32 v3, v3, v2
	s_waitcnt lgkmcnt(1)
	v_max_f32_e32 v5, v5, v5
	s_waitcnt lgkmcnt(0)
	v_max_f32_e32 v3, v3, v3
	v_max_f32_e32 v2, v2, v3
	v_xor_b32_e32 v3, 1, v177
	v_cmp_lt_i32_e32 vcc, v3, v6
	v_max_f32_e32 v4, v4, v5
	s_nop 0
	v_cndmask_b32_e32 v3, v177, v3, vcc
	v_lshlrev_b32_e32 v3, 2, v3
	ds_bpermute_b32 v5, v3, v4
	ds_bpermute_b32 v3, v3, v2
	s_waitcnt lgkmcnt(1)
	v_max_f32_e32 v5, v5, v5
	v_max_f32_e32 v4, v4, v5
	s_waitcnt lgkmcnt(0)
	v_max_f32_e32 v3, v3, v3
	v_max_f32_e32 v2, v2, v3
	v_mul_f32_e32 v3, 0xc13c5bb7, v4
	v_mul_f32_e32 v2, v2, v3
	s_nop 0
	v_readfirstlane_b32 s11, v2
	s_nop 0
	s_mov_b32 s101, s11
	s_mov_b32 s100, 1
.Lnegc_done_a:
	s_cbranch_scc1 .LBB0_642
	s_setprio 1

.LBB0_689:
	s_andn2_b64 vcc, exec, s[4:5]
	s_cbranch_vccnz .LBB0_697
	s_cmp_lg_u32 s100, 0
	s_cbranch_scc0 .Lnegc_calc_b
	v_mov_b32_e32 v50, v0
	s_nop 0
	v_readfirstlane_b32 s11, v50
	s_mov_b32 s13, s101
	s_ashr_i32 s1, s11, 6
	s_cmp_lt_i32 s1, 4
	s_branch .Lnegc_done_b
.Lnegc_calc_b:
	v_mov_b32_e32 v2, v0
	s_load_dwordx4 s[4:7], s[66:67], 0x48
	v_readlane_b32 s10, v254, 30
	v_and_b32_e32 v6, 64, v177
	v_add_u32_e32 v6, 64, v6
	v_and_or_b32 v130, v2, 63, s10
	v_lshlrev_b64 v[2:3], 2, v[130:131]
	s_waitcnt lgkmcnt(0)
	v_lshl_add_u64 v[4:5], s[4:5], 0, v[2:3]
	v_lshl_add_u64 v[2:3], s[6:7], 0, v[2:3]
	global_load_dword v2, v[2:3], off
	v_xor_b32_e32 v7, 32, v177
	global_load_dword v4, v[4:5], off
	v_cmp_lt_i32_e32 vcc, v7, v6
	v_readlane_b32 s11, v254, 31
	v_mov_b32_e32 v50, v0
	v_cndmask_b32_e32 v7, v177, v7, vcc
	v_lshlrev_b32_e32 v7, 2, v7
	s_waitcnt vmcnt(0)
	v_and_b32_e32 v3, 0x7fffffff, v2
	ds_bpermute_b32 v3, v7, v3
	v_and_b32_e32 v5, 0x7fffffff, v4
	ds_bpermute_b32 v5, v7, v5
	v_max_f32_e64 v2, |v2|, |v2|
	v_max_f32_e64 v4, |v4|, |v4|
	s_waitcnt lgkmcnt(1)
	v_max_f32_e32 v3, v3, v3
	v_max_f32_e32 v2, v2, v3
	v_xor_b32_e32 v3, 16, v177
	v_cmp_lt_i32_e32 vcc, v3, v6
	s_waitcnt lgkmcnt(0)
	v_max_f32_e32 v5, v5, v5
	v_max_f32_e32 v4, v4, v5
	v_cndmask_b32_e32 v3, v177, v3, vcc
	v_lshlrev_b32_e32 v3, 2, v3
	ds_bpermute_b32 v5, v3, v4
	ds_bpermute_b32 v3, v3, v2
	v_readfirstlane_b32 s11, v50
	s_ashr_i32 s1, s11, 6
	s_cmp_lt_i32 s1, 4
	s_waitcnt lgkmcnt(1)
	v_max_f32_e32 v5, v5, v5
	s_waitcnt lgkmcnt(0)
	v_max_f32_e32 v3, v3, v3
	v_max_f32_e32 v2, v2, v3
	v_xor_b32_e32 v3, 8, v177
	v_cmp_lt_i32_e32 vcc, v3, v6
	v_max_f32_e32 v4, v4, v5
	s_nop 0
	v_cndmask_b32_e32 v3, v177, v3, vcc
	v_lshlrev_b32_e32 v3, 2, v3
	ds_bpermute_b32 v5, v3, v4
	ds_bpermute_b32 v3, v3, v2
	s_waitcnt lgkmcnt(1)
	v_max_f32_e32 v5, v5, v5
	s_waitcnt lgkmcnt(0)
	v_max_f32_e32 v3, v3, v3
	v_max_f32_e32 v2, v2, v3
	v_xor_b32_e32 v3, 4, v177
	v_cmp_lt_i32_e32 vcc, v3, v6
	v_max_f32_e32 v4, v4, v5
	s_nop 0
	v_cndmask_b32_e32 v3, v177, v3, vcc
	v_lshlrev_b32_e32 v3, 2, v3
	ds_bpermute_b32 v5, v3, v4
	ds_bpermute_b32 v3, v3, v2
	s_waitcnt lgkmcnt(1)
	v_max_f32_e32 v5, v5, v5
	s_waitcnt lgkmcnt(0)
	v_max_f32_e32 v3, v3, v3
	v_max_f32_e32 v2, v2, v3
	v_xor_b32_e32 v3, 2, v177
	v_cmp_lt_i32_e32 vcc, v3, v6
	v_max_f32_e32 v4, v4, v5
	s_nop 0
	v_cndmask_b32_e32 v3, v177, v3, vcc
	v_lshlrev_b32_e32 v3, 2, v3
	ds_bpermute_b32 v5, v3, v4
	ds_bpermute_b32 v3, v3, v2
	s_waitcnt lgkmcnt(1)
	v_max_f32_e32 v5, v5, v5
	s_waitcnt lgkmcnt(0)
	v_max_f32_e32 v3, v3, v3
	v_max_f32_e32 v2, v2, v3
	v_xor_b32_e32 v3, 1, v177
	v_cmp_lt_i32_e32 vcc, v3, v6
	v_max_f32_e32 v4, v4, v5
	s_nop 0
	v_cndmask_b32_e32 v3, v177, v3, vcc
	v_lshlrev_b32_e32 v3, 2, v3
	ds_bpermute_b32 v5, v3, v4
	ds_bpermute_b32 v3, v3, v2
	s_waitcnt lgkmcnt(1)
	v_max_f32_e32 v5, v5, v5
	v_max_f32_e32 v4, v4, v5
	s_waitcnt lgkmcnt(0)
	v_max_f32_e32 v3, v3, v3
	v_max_f32_e32 v2, v2, v3
	v_mul_f32_e32 v3, 0xc13c5bb7, v4
	v_mul_f32_e32 v2, v2, v3
	s_nop 0
	v_readfirstlane_b32 s13, v2
	s_nop 0
	s_mov_b32 s101, s13
	s_mov_b32 s100, 1

.LBB0_1261:
	s_or_b64 exec, exec, s[16:17]
	v_lshlrev_b32_e32 v109, 16, v102
	v_lshlrev_b32_e32 v108, 16, v106
	v_lshlrev_b32_e32 v111, 16, v100
	v_lshlrev_b32_e32 v110, 16, v104
	s_waitcnt lgkmcnt(3)
	v_pk_fma_f32 v[112:113], v[14:15], v[110:111], v[108:109] op_sel_hi:[0,1,1]
	v_and_b32_e32 v109, 0xffff0000, v102
	v_and_b32_e32 v108, 0xffff0000, v106
	v_and_b32_e32 v111, 0xffff0000, v100
	v_and_b32_e32 v110, 0xffff0000, v104
	v_pk_fma_f32 v[116:117], v[14:15], v[110:111], v[108:109] op_sel:[1,0,0]
	v_lshlrev_b32_e32 v15, 16, v103
	v_lshlrev_b32_e32 v14, 16, v107
	v_lshlrev_b32_e32 v109, 16, v101
	v_lshlrev_b32_e32 v108, 16, v105
	v_pk_fma_f32 v[140:141], v[16:17], v[108:109], v[14:15] op_sel_hi:[0,1,1]
	v_and_b32_e32 v15, 0xffff0000, v103
	v_and_b32_e32 v14, 0xffff0000, v107
	v_and_b32_e32 v101, 0xffff0000, v101
	v_and_b32_e32 v100, 0xffff0000, v105
	v_mov_b32_e32 v16, v17
	v_pk_fma_f32 v[16:17], v[16:17], v[100:101], v[14:15] op_sel_hi:[0,1,1]
	v_pk_mul_f32 v[14:15], v[116:117], v[116:117]
	v_lshlrev_b32_e32 v101, 16, v92
	v_pk_fma_f32 v[14:15], v[112:113], v[112:113], v[14:15]
	v_lshlrev_b32_e32 v100, 16, v96
	v_pk_fma_f32 v[14:15], v[140:141], v[140:141], v[14:15]
	s_mov_b32 s16, 0x3a800000
	v_pk_fma_f32 v[104:105], v[16:17], v[16:17], v[14:15]
	v_lshlrev_b32_e32 v15, 16, v94
	v_lshlrev_b32_e32 v14, 16, v98
	s_waitcnt lgkmcnt(2)
	v_pk_fma_f32 v[102:103], v[10:11], v[100:101], v[14:15] op_sel_hi:[0,1,1]
	v_and_b32_e32 v15, 0xffff0000, v94
	v_and_b32_e32 v14, 0xffff0000, v98
	v_and_b32_e32 v101, 0xffff0000, v92
	v_and_b32_e32 v100, 0xffff0000, v96
	v_pk_fma_f32 v[106:107], v[10:11], v[100:101], v[14:15] op_sel:[1,0,0]
	v_lshlrev_b32_e32 v11, 16, v95
	v_lshlrev_b32_e32 v10, 16, v99
	v_lshlrev_b32_e32 v15, 16, v93
	v_lshlrev_b32_e32 v14, 16, v97
	v_pk_fma_f32 v[108:109], v[12:13], v[14:15], v[10:11] op_sel_hi:[0,1,1]
	v_and_b32_e32 v11, 0xffff0000, v95
	v_and_b32_e32 v10, 0xffff0000, v99
	v_and_b32_e32 v15, 0xffff0000, v93
	v_and_b32_e32 v14, 0xffff0000, v97
	v_mov_b32_e32 v12, v13
	v_pk_fma_f32 v[110:111], v[12:13], v[14:15], v[10:11] op_sel_hi:[0,1,1]
	v_pk_mul_f32 v[10:11], v[106:107], v[106:107]
	v_lshlrev_b32_e32 v13, 16, v84
	v_pk_fma_f32 v[10:11], v[102:103], v[102:103], v[10:11]
	v_lshlrev_b32_e32 v12, 16, v88
	v_pk_fma_f32 v[10:11], v[108:109], v[108:109], v[10:11]
	v_and_b32_e32 v15, 0xffff0000, v84
	v_pk_fma_f32 v[94:95], v[110:111], v[110:111], v[10:11]
	v_lshlrev_b32_e32 v11, 16, v86
	v_lshlrev_b32_e32 v10, 16, v90
	s_waitcnt lgkmcnt(1)
	v_pk_fma_f32 v[10:11], v[6:7], v[12:13], v[10:11] op_sel_hi:[0,1,1]
	v_and_b32_e32 v13, 0xffff0000, v86
	v_and_b32_e32 v12, 0xffff0000, v90
	v_and_b32_e32 v14, 0xffff0000, v88
	v_pk_fma_f32 v[12:13], v[6:7], v[14:15], v[12:13] op_sel:[1,0,0]
	v_lshlrev_b32_e32 v7, 16, v87
	v_lshlrev_b32_e32 v6, 16, v91
	v_lshlrev_b32_e32 v15, 16, v85
	v_lshlrev_b32_e32 v14, 16, v89
	v_pk_fma_f32 v[98:99], v[8:9], v[14:15], v[6:7] op_sel_hi:[0,1,1]
	v_pk_mul_f32 v[6:7], v[12:13], v[12:13]
	v_and_b32_e32 v15, 0xffff0000, v85
	v_pk_fma_f32 v[6:7], v[10:11], v[10:11], v[6:7]
	v_and_b32_e32 v14, 0xffff0000, v89
	v_pk_fma_f32 v[96:97], v[98:99], v[98:99], v[6:7]
	v_and_b32_e32 v7, 0xffff0000, v87
	v_and_b32_e32 v6, 0xffff0000, v91
	v_mov_b32_e32 v8, v9
	v_pk_fma_f32 v[100:101], v[8:9], v[14:15], v[6:7] op_sel_hi:[0,1,1]
	v_and_b32_e32 v7, 0xffff0000, v79
	v_and_b32_e32 v6, 0xffff0000, v83
	v_and_b32_e32 v9, 0xffff0000, v77
	v_and_b32_e32 v8, 0xffff0000, v81
	s_waitcnt lgkmcnt(0)
	v_mov_b32_e32 v14, v5
	v_pk_fma_f32 v[6:7], v[14:15], v[8:9], v[6:7] op_sel_hi:[0,1,1]
	v_lshlrev_b32_e32 v9, 16, v78
	v_lshlrev_b32_e32 v8, 16, v82
	v_lshlrev_b32_e32 v15, 16, v76
	v_lshlrev_b32_e32 v14, 16, v80
	v_pk_fma_f32 v[14:15], v[2:3], v[14:15], v[8:9] op_sel_hi:[0,1,1]
	v_and_b32_e32 v9, 0xffff0000, v78
	v_and_b32_e32 v8, 0xffff0000, v82
	v_and_b32_e32 v85, 0xffff0000, v76
	v_and_b32_e32 v84, 0xffff0000, v80
	v_pk_fma_f32 v[90:91], v[2:3], v[84:85], v[8:9] op_sel:[1,0,0]
	v_lshlrev_b32_e32 v9, 16, v79
	v_pk_mul_f32 v[2:3], v[90:91], v[90:91]
	v_lshlrev_b32_e32 v8, 16, v83
	v_lshlrev_b32_e32 v77, 16, v77
	v_lshlrev_b32_e32 v76, 16, v81
	v_pk_fma_f32 v[2:3], v[14:15], v[14:15], v[2:3]
	v_pk_fma_f32 v[92:93], v[4:5], v[76:77], v[8:9] op_sel_hi:[0,1,1]
	v_pk_add_f32 v[4:5], v[104:105], v[94:95]
	v_pk_fma_f32 v[8:9], v[100:101], v[100:101], v[96:97]
	v_pk_fma_f32 v[2:3], v[92:93], v[92:93], v[2:3]
	v_pk_add_f32 v[4:5], v[4:5], v[8:9]
	v_pk_fma_f32 v[2:3], v[6:7], v[6:7], v[2:3]
	s_nop 0
	v_pk_add_f32 v[2:3], v[4:5], v[2:3]
	s_nop 1
	v_add_f32_dpp v2, v2, v2 quad_perm:[1,0,3,2] row_mask:0xf bank_mask:0xf
	v_add_f32_dpp v3, v3, v3 quad_perm:[1,0,3,2] row_mask:0xf bank_mask:0xf
	s_nop 0
	v_add_f32_dpp v2, v2, v2 quad_perm:[2,3,0,1] row_mask:0xf bank_mask:0xf
	v_add_f32_dpp v3, v3, v3 quad_perm:[2,3,0,1] row_mask:0xf bank_mask:0xf
	s_nop 0
	v_add_f32_dpp v2, v2, v2 row_half_mirror row_mask:0xf bank_mask:0xf
	v_add_f32_dpp v3, v3, v3 row_half_mirror row_mask:0xf bank_mask:0xf
	s_nop 0
	v_add_f32_dpp v2, v2, v2 row_mirror row_mask:0xf bank_mask:0xf
	v_add_f32_dpp v3, v3, v3 row_mirror row_mask:0xf bank_mask:0xf
	s_nop 0
	v_add_f32_dpp v2, v2, v2 row_bcast:15 row_mask:0xa bank_mask:0xf
	v_add_f32_dpp v3, v3, v3 row_bcast:15 row_mask:0xa bank_mask:0xf
	s_nop 0
	v_add_f32_dpp v2, v2, v2 row_bcast:31 row_mask:0xc bank_mask:0xf
	v_add_f32_dpp v3, v3, v3 row_bcast:31 row_mask:0xc bank_mask:0xf
	s_nop 0
	v_readlane_b32 s100, v2, 63
	v_readlane_b32 s101, v3, 63
	s_nop 1
	v_mov_b32_e32 v2, s100
	v_mov_b32_e32 v3, s101
	s_nop 0
	v_pk_fma_f32 v[2:3], v[2:3], s[16:17], v[176:177] op_sel_hi:[1,0,0]
	s_nop 0
	v_mul_f32_e32 v4, 0x4b800000, v3
	v_cmp_gt_f32_e32 vcc, s25, v3
	v_cmp_gt_f32_e64 s[16:17], s25, v2
	s_nop 0
	v_cndmask_b32_e32 v3, v3, v4, vcc
	v_mul_f32_e32 v4, 0x4b800000, v2
	v_rsq_f32_e32 v3, v3
	v_cndmask_b32_e64 v2, v2, v4, s[16:17]
	v_rsq_f32_e32 v2, v2
	v_mul_f32_e32 v4, 0x45800000, v3
	v_cndmask_b32_e32 v4, v3, v4, vcc
	v_mul_f32_e32 v3, 0x45800000, v2
	v_cndmask_b32_e64 v104, v2, v3, s[16:17]
	ds_read_b128 v[76:79], v121
	ds_read_b128 v[86:89], v122
	v_mov_b32_e32 v2, v113
	v_mov_b32_e32 v3, v117
	v_pk_mul_f32 v[2:3], v[2:3], v[4:5] op_sel_hi:[1,0]
	v_mov_b32_e32 v8, v141
	v_mov_b32_e32 v9, v17
	s_waitcnt lgkmcnt(0)
	v_pk_fma_f32 v[94:95], v[76:77], v[2:3], v[86:87]
	v_pk_mul_f32 v[8:9], v[8:9], v[4:5] op_sel_hi:[1,0]
	v_med3_f32 v2, v94, s26, v209
	v_med3_f32 v3, v95, s26, v209
	v_mov_b32_e32 v5, v131
	v_cvt_pk_fp8_f32 v5, v2, v3
	v_pk_fma_f32 v[82:83], v[78:79], v[8:9], v[88:89]
	s_mov_b32 s16, 0x41068000
	v_med3_f32 v2, v82, s26, v209
	v_med3_f32 v3, v83, s26, v209
	v_cvt_pk_fp8_f32 v5, v2, v3 op_sel:[0,0,1]
	v_lshl_add_u64 v[2:3], s[62:63], 0, v[40:41]
	v_add_co_u32_e32 v114, vcc, s16, v2
	v_mov_b32_e32 v113, v116
	s_nop 0
	v_addc_co_u32_e32 v115, vcc, 0, v3, vcc
	v_pk_mul_f32 v[2:3], v[112:113], v[104:105] op_sel_hi:[1,0]
	global_store_dword v[114:115], v5, off
	v_pk_fma_f32 v[96:97], v[76:77], v[2:3], v[86:87]
	v_mov_b32_e32 v5, v131
	v_med3_f32 v2, v96, s26, v209
	v_med3_f32 v3, v97, s26, v209
	v_mov_b32_e32 v141, v16
	v_cvt_pk_fp8_f32 v5, v2, v3
	v_pk_mul_f32 v[8:9], v[140:141], v[104:105] op_sel_hi:[1,0]
	s_nop 0
	v_pk_fma_f32 v[84:85], v[78:79], v[8:9], v[88:89]
	s_nop 0
	v_med3_f32 v2, v84, s26, v209
	v_med3_f32 v3, v85, s26, v209
	v_cvt_pk_fp8_f32 v5, v2, v3 op_sel:[0,0,1]
	v_add_u32_e32 v2, -16, v36
	v_ashrrev_i32_e32 v3, 31, v2
	v_lshlrev_b64 v[8:9], 10, v[2:3]
	v_lshl_add_u64 v[16:17], v[26:27], 0, v[8:9]
	global_store_dword v[16:17], v5, off
	ds_read_b128 v[78:81], v123
	ds_read_b128 v[140:143], v124
	v_mov_b32_e32 v16, v103
	v_mov_b32_e32 v17, v107
	v_pk_mul_f32 v[76:77], v[16:17], v[4:5] op_sel_hi:[1,0]
	v_mov_b32_e32 v16, v109
	v_mov_b32_e32 v17, v111
	s_waitcnt lgkmcnt(0)
	v_pk_fma_f32 v[86:87], v[76:77], v[78:79], v[140:141]
	v_pk_mul_f32 v[16:17], v[16:17], v[4:5] op_sel_hi:[1,0]
	v_med3_f32 v5, v86, s26, v209
	v_med3_f32 v37, v87, s26, v209
	v_mov_b32_e32 v76, v131
	v_cvt_pk_fp8_f32 v76, v5, v37
	v_pk_fma_f32 v[16:17], v[16:17], v[80:81], v[142:143]
	v_mov_b32_e32 v103, v106
	v_med3_f32 v5, v16, s26, v209
	v_med3_f32 v37, v17, s26, v209
	v_cvt_pk_fp8_f32 v76, v5, v37 op_sel:[0,0,1]
	v_pk_mul_f32 v[88:89], v[102:103], v[104:105] op_sel_hi:[1,0]
	v_mov_b32_e32 v109, v110
	v_pk_fma_f32 v[88:89], v[88:89], v[78:79], v[140:141]
	v_mov_b32_e32 v78, v131
	v_med3_f32 v5, v88, s26, v209
	v_med3_f32 v37, v89, s26, v209
	v_cvt_pk_fp8_f32 v78, v5, v37
	global_store_dword v[114:115], v76, off offset:256
	v_pk_mul_f32 v[76:77], v[108:109], v[104:105] op_sel_hi:[1,0]
	v_lshl_add_u64 v[102:103], s[64:65], 0, v[8:9]
	v_pk_fma_f32 v[76:77], v[76:77], v[80:81], v[142:143]
	v_lshl_add_u64 v[8:9], v[102:103], 0, v[28:29]
	v_med3_f32 v5, v76, s26, v209
	v_med3_f32 v37, v77, s26, v209
	v_cvt_pk_fp8_f32 v78, v5, v37 op_sel:[0,0,1]
	v_mov_b32_e32 v37, v131
	global_store_dword v[8:9], v78, off
	ds_read_b128 v[106:109], v125
	ds_read_b128 v[110:113], v126
	v_mov_b32_e32 v8, v11
	v_mov_b32_e32 v9, v13
	v_pk_mul_f32 v[78:79], v[8:9], v[4:5] op_sel_hi:[1,0]
	v_mov_b32_e32 v8, v99
	v_mov_b32_e32 v9, v101
	s_waitcnt lgkmcnt(0)
	v_pk_fma_f32 v[78:79], v[78:79], v[106:107], v[110:111]
	v_pk_mul_f32 v[8:9], v[8:9], v[4:5] op_sel_hi:[1,0]
	v_med3_f32 v5, v78, s26, v209
	v_med3_f32 v11, v79, s26, v209
	v_mov_b32_e32 v13, v131
	v_cvt_pk_fp8_f32 v13, v5, v11
	v_pk_fma_f32 v[8:9], v[8:9], v[108:109], v[112:113]
	v_mov_b32_e32 v99, v100
	v_med3_f32 v5, v8, s26, v209
	v_med3_f32 v11, v9, s26, v209
	v_cvt_pk_fp8_f32 v13, v5, v11 op_sel:[0,0,1]
	v_mov_b32_e32 v11, v12
	v_pk_mul_f32 v[10:11], v[10:11], v[104:105] op_sel_hi:[1,0]
	global_store_dword v[114:115], v13, off offset:512
	v_pk_fma_f32 v[80:81], v[10:11], v[106:107], v[110:111]
	v_pk_mul_f32 v[12:13], v[98:99], v[104:105] op_sel_hi:[1,0]
	v_med3_f32 v5, v80, s26, v209
	v_med3_f32 v10, v81, s26, v209
	v_cvt_pk_fp8_f32 v37, v5, v10
	v_pk_fma_f32 v[12:13], v[12:13], v[108:109], v[112:113]
	v_mov_b32_e32 v111, v7
	v_med3_f32 v5, v12, s26, v209
	v_med3_f32 v10, v13, s26, v209
	v_cvt_pk_fp8_f32 v37, v5, v10 op_sel:[0,0,1]
	v_lshl_add_u64 v[10:11], v[102:103], 0, v[30:31]
	v_mov_b32_e32 v110, v93
	v_mov_b32_e32 v93, v6
	global_store_dword v[10:11], v37, off
	ds_read_b128 v[98:101], v127
	ds_read_b128 v[106:109], v128
	v_mov_b32_e32 v10, v15
	v_mov_b32_e32 v11, v91
	v_pk_mul_f32 v[10:11], v[10:11], v[4:5] op_sel_hi:[1,0]
	v_mov_b32_e32 v37, v131
	s_waitcnt lgkmcnt(0)
	v_pk_fma_f32 v[10:11], v[10:11], v[98:99], v[106:107]
	v_pk_mul_f32 v[4:5], v[110:111], v[4:5] op_sel_hi:[1,0]
	v_med3_f32 v7, v10, s26, v209
	v_med3_f32 v15, v11, s26, v209
	v_cvt_pk_fp8_f32 v37, v7, v15
	v_pk_fma_f32 v[4:5], v[4:5], v[100:101], v[108:109]
	s_nop 0
	v_med3_f32 v7, v4, s26, v209
	v_med3_f32 v15, v5, s26, v209
	v_cvt_pk_fp8_f32 v37, v7, v15 op_sel:[0,0,1]
	v_mov_b32_e32 v15, v90
	v_pk_mul_f32 v[14:15], v[14:15], v[104:105] op_sel_hi:[1,0]
	v_pk_mul_f32 v[6:7], v[92:93], v[104:105] op_sel_hi:[1,0]
	v_pk_fma_f32 v[14:15], v[14:15], v[98:99], v[106:107]
	global_store_dword v[114:115], v37, off offset:768
	v_med3_f32 v37, v14, s26, v209
	v_med3_f32 v90, v15, s26, v209
	v_mov_b32_e32 v92, v131
	v_cvt_pk_fp8_f32 v92, v37, v90
	v_pk_fma_f32 v[6:7], v[6:7], v[100:101], v[108:109]
	s_nop 0
	v_med3_f32 v37, v6, s26, v209
	v_med3_f32 v90, v7, s26, v209
	v_cvt_pk_fp8_f32 v92, v37, v90 op_sel:[0,0,1]
	v_lshl_add_u64 v[90:91], v[102:103], 0, v[32:33]
	global_store_dword v[90:91], v92, off
	v_mov_b32_e32 v37, v120
	v_mov_b32_e32 v110, v94
	v_add_u32_e32 v37, 0, v37
	ds_read_b128 v[90:93], v37
	ds_read_b128 v[98:101], v37 offset:16
	ds_read_b128 v[102:105], v37 offset:32
	ds_read_b128 v[106:109], v37 offset:48
	v_mov_b32_e32 v111, v96
	s_waitcnt lgkmcnt(3)
	v_pk_fma_f32 v[112:113], v[110:111], v[90:91], 0 op_sel_hi:[1,0,0]
	v_pk_fma_f32 v[114:115], v[110:111], v[90:91], 0 op_sel:[0,1,0] op_sel_hi:[1,1,0]
	v_mov_b32_e32 v90, v93
	v_pk_fma_f32 v[140:141], v[110:111], v[90:91], 0 op_sel_hi:[1,0,0]
	s_waitcnt lgkmcnt(2)
	v_mov_b32_e32 v90, v101
	v_pk_fma_f32 v[148:149], v[110:111], v[90:91], 0 op_sel_hi:[1,0,0]
	s_waitcnt lgkmcnt(1)
	v_mov_b32_e32 v90, v105
	v_pk_fma_f32 v[156:157], v[110:111], v[90:91], 0 op_sel_hi:[1,0,0]
	s_waitcnt lgkmcnt(0)
	v_mov_b32_e32 v90, v109
	v_pk_fma_f32 v[116:117], v[110:111], v[92:93], 0 op_sel_hi:[1,0,0]
	v_pk_fma_f32 v[142:143], v[110:111], v[98:99], 0 op_sel_hi:[1,0,0]
	v_pk_fma_f32 v[144:145], v[110:111], v[98:99], 0 op_sel:[0,1,0] op_sel_hi:[1,1,0]
	v_pk_fma_f32 v[146:147], v[110:111], v[100:101], 0 op_sel_hi:[1,0,0]
	v_pk_fma_f32 v[150:151], v[110:111], v[102:103], 0 op_sel_hi:[1,0,0]
	v_pk_fma_f32 v[152:153], v[110:111], v[102:103], 0 op_sel:[0,1,0] op_sel_hi:[1,1,0]
	v_pk_fma_f32 v[154:155], v[110:111], v[104:105], 0 op_sel_hi:[1,0,0]
	v_pk_fma_f32 v[158:159], v[110:111], v[106:107], 0 op_sel_hi:[1,0,0]
	v_pk_fma_f32 v[160:161], v[110:111], v[106:107], 0 op_sel:[0,1,0] op_sel_hi:[1,1,0]
	v_pk_fma_f32 v[162:163], v[110:111], v[108:109], 0 op_sel_hi:[1,0,0]
	v_pk_fma_f32 v[110:111], v[110:111], v[90:91], 0 op_sel_hi:[1,0,0]
	ds_read_b128 v[90:93], v37 offset:20480
	ds_read_b128 v[98:101], v37 offset:20496
	ds_read_b128 v[102:105], v37 offset:20512
	ds_read_b128 v[106:109], v37 offset:20528
	v_mov_b32_e32 v96, v95
	s_waitcnt lgkmcnt(3)
	v_pk_fma_f32 v[112:113], v[96:97], v[90:91], v[112:113] op_sel_hi:[1,0,1]
	v_pk_fma_f32 v[114:115], v[96:97], v[90:91], v[114:115] op_sel:[0,1,0]
	v_mov_b32_e32 v90, v93
	v_pk_fma_f32 v[140:141], v[96:97], v[90:91], v[140:141] op_sel_hi:[1,0,1]
	s_waitcnt lgkmcnt(2)
	v_mov_b32_e32 v90, v101
	v_pk_fma_f32 v[148:149], v[96:97], v[90:91], v[148:149] op_sel_hi:[1,0,1]
	s_waitcnt lgkmcnt(1)
	v_mov_b32_e32 v90, v105
	v_pk_fma_f32 v[156:157], v[96:97], v[90:91], v[156:157] op_sel_hi:[1,0,1]
	s_waitcnt lgkmcnt(0)
	v_mov_b32_e32 v90, v109
	v_pk_fma_f32 v[116:117], v[96:97], v[92:93], v[116:117] op_sel_hi:[1,0,1]
	v_pk_fma_f32 v[142:143], v[96:97], v[98:99], v[142:143] op_sel_hi:[1,0,1]
	v_pk_fma_f32 v[144:145], v[96:97], v[98:99], v[144:145] op_sel:[0,1,0]
	v_pk_fma_f32 v[146:147], v[96:97], v[100:101], v[146:147] op_sel_hi:[1,0,1]
	v_pk_fma_f32 v[150:151], v[96:97], v[102:103], v[150:151] op_sel_hi:[1,0,1]
	v_pk_fma_f32 v[152:153], v[96:97], v[102:103], v[152:153] op_sel:[0,1,0]
	v_pk_fma_f32 v[154:155], v[96:97], v[104:105], v[154:155] op_sel_hi:[1,0,1]
	v_pk_fma_f32 v[158:159], v[96:97], v[106:107], v[158:159] op_sel_hi:[1,0,1]
	v_pk_fma_f32 v[106:107], v[96:97], v[106:107], v[160:161] op_sel:[0,1,0]
	v_pk_fma_f32 v[160:161], v[96:97], v[108:109], v[162:163] op_sel_hi:[1,0,1]
	v_pk_fma_f32 v[108:109], v[96:97], v[90:91], v[110:111] op_sel_hi:[1,0,1]
	ds_read_b128 v[90:93], v37 offset:40960
	ds_read_b128 v[94:97], v37 offset:40976
	ds_read_b128 v[98:101], v37 offset:40992
	ds_read_b128 v[102:105], v37 offset:41008
	v_mov_b32_e32 v110, v82
	v_mov_b32_e32 v111, v84
	s_waitcnt lgkmcnt(3)
	v_mov_b32_e32 v82, v93
	v_pk_fma_f32 v[140:141], v[110:111], v[82:83], v[140:141] op_sel_hi:[1,0,1]
	s_waitcnt lgkmcnt(2)
	v_mov_b32_e32 v82, v97
	v_pk_fma_f32 v[148:149], v[110:111], v[82:83], v[148:149] op_sel_hi:[1,0,1]
	s_waitcnt lgkmcnt(1)
	v_mov_b32_e32 v82, v101
	v_pk_fma_f32 v[156:157], v[110:111], v[82:83], v[156:157] op_sel_hi:[1,0,1]
	s_waitcnt lgkmcnt(0)
	v_mov_b32_e32 v82, v105
	v_pk_fma_f32 v[112:113], v[110:111], v[90:91], v[112:113] op_sel_hi:[1,0,1]
	v_pk_fma_f32 v[114:115], v[110:111], v[90:91], v[114:115] op_sel:[0,1,0]
	v_pk_fma_f32 v[116:117], v[110:111], v[92:93], v[116:117] op_sel_hi:[1,0,1]
	v_pk_fma_f32 v[142:143], v[110:111], v[94:95], v[142:143] op_sel_hi:[1,0,1]
	v_pk_fma_f32 v[144:145], v[110:111], v[94:95], v[144:145] op_sel:[0,1,0]
	v_pk_fma_f32 v[146:147], v[110:111], v[96:97], v[146:147] op_sel_hi:[1,0,1]
	v_pk_fma_f32 v[150:151], v[110:111], v[98:99], v[150:151] op_sel_hi:[1,0,1]
	v_pk_fma_f32 v[152:153], v[110:111], v[98:99], v[152:153] op_sel:[0,1,0]
	v_pk_fma_f32 v[154:155], v[110:111], v[100:101], v[154:155] op_sel_hi:[1,0,1]
	v_pk_fma_f32 v[158:159], v[110:111], v[102:103], v[158:159] op_sel_hi:[1,0,1]
	v_pk_fma_f32 v[106:107], v[110:111], v[102:103], v[106:107] op_sel:[0,1,0]
	v_pk_fma_f32 v[160:161], v[110:111], v[104:105], v[160:161] op_sel_hi:[1,0,1]
	v_pk_fma_f32 v[108:109], v[110:111], v[82:83], v[108:109] op_sel_hi:[1,0,1]
	ds_read_b128 v[90:93], v37 offset:61440
	ds_read_b128 v[94:97], v37 offset:61456
	ds_read_b128 v[98:101], v37 offset:61472
	ds_read_b128 v[102:105], v37 offset:61488
	v_mov_b32_e32 v84, v83
	s_waitcnt lgkmcnt(3)
	v_mov_b32_e32 v82, v93
	v_pk_fma_f32 v[110:111], v[84:85], v[90:91], v[112:113] op_sel_hi:[1,0,1]
	v_pk_fma_f32 v[112:113], v[84:85], v[90:91], v[114:115] op_sel:[0,1,0]
	v_pk_fma_f32 v[114:115], v[84:85], v[92:93], v[116:117] op_sel_hi:[1,0,1]
	v_pk_fma_f32 v[116:117], v[84:85], v[82:83], v[140:141] op_sel_hi:[1,0,1]
	s_waitcnt lgkmcnt(2)
	v_mov_b32_e32 v82, v97
	v_pk_fma_f32 v[140:141], v[84:85], v[94:95], v[142:143] op_sel_hi:[1,0,1]
	v_pk_fma_f32 v[142:143], v[84:85], v[94:95], v[144:145] op_sel:[0,1,0]
	v_pk_fma_f32 v[144:145], v[84:85], v[96:97], v[146:147] op_sel_hi:[1,0,1]
	v_pk_fma_f32 v[146:147], v[84:85], v[82:83], v[148:149] op_sel_hi:[1,0,1]
	s_waitcnt lgkmcnt(1)
	v_mov_b32_e32 v82, v101
	v_pk_fma_f32 v[148:149], v[84:85], v[98:99], v[150:151] op_sel_hi:[1,0,1]
	v_pk_fma_f32 v[150:151], v[84:85], v[98:99], v[152:153] op_sel:[0,1,0]
	v_pk_fma_f32 v[152:153], v[84:85], v[100:101], v[154:155] op_sel_hi:[1,0,1]
	v_pk_fma_f32 v[154:155], v[84:85], v[82:83], v[156:157] op_sel_hi:[1,0,1]
	s_waitcnt lgkmcnt(0)
	v_mov_b32_e32 v82, v105
	v_pk_fma_f32 v[156:157], v[84:85], v[102:103], v[158:159] op_sel_hi:[1,0,1]
	v_pk_fma_f32 v[102:103], v[84:85], v[102:103], v[106:107] op_sel:[0,1,0]
	v_pk_fma_f32 v[106:107], v[84:85], v[104:105], v[160:161] op_sel_hi:[1,0,1]
	v_pk_fma_f32 v[104:105], v[84:85], v[82:83], v[108:109] op_sel_hi:[1,0,1]
	ds_read_b128 v[82:85], v37 offset:5120
	ds_read_b128 v[90:93], v37 offset:5136
	ds_read_b128 v[94:97], v37 offset:5152
	ds_read_b128 v[98:101], v37 offset:5168
	v_mov_b32_e32 v108, v86
	v_mov_b32_e32 v109, v88
	s_waitcnt lgkmcnt(3)
	v_pk_fma_f32 v[110:111], v[108:109], v[82:83], v[110:111] op_sel_hi:[1,0,1]
	v_pk_fma_f32 v[112:113], v[108:109], v[82:83], v[112:113] op_sel:[0,1,0]
	v_mov_b32_e32 v82, v85
	v_pk_fma_f32 v[116:117], v[108:109], v[82:83], v[116:117] op_sel_hi:[1,0,1]
	s_waitcnt lgkmcnt(2)
	v_mov_b32_e32 v82, v93
	v_pk_fma_f32 v[146:147], v[108:109], v[82:83], v[146:147] op_sel_hi:[1,0,1]
	s_waitcnt lgkmcnt(1)
	v_mov_b32_e32 v82, v97
	v_pk_fma_f32 v[154:155], v[108:109], v[82:83], v[154:155] op_sel_hi:[1,0,1]
	s_waitcnt lgkmcnt(0)
	v_mov_b32_e32 v82, v101
	v_pk_fma_f32 v[114:115], v[108:109], v[84:85], v[114:115] op_sel_hi:[1,0,1]
	v_pk_fma_f32 v[140:141], v[108:109], v[90:91], v[140:141] op_sel_hi:[1,0,1]
	v_pk_fma_f32 v[142:143], v[108:109], v[90:91], v[142:143] op_sel:[0,1,0]
	v_pk_fma_f32 v[144:145], v[108:109], v[92:93], v[144:145] op_sel_hi:[1,0,1]
	v_pk_fma_f32 v[148:149], v[108:109], v[94:95], v[148:149] op_sel_hi:[1,0,1]
	v_pk_fma_f32 v[150:151], v[108:109], v[94:95], v[150:151] op_sel:[0,1,0]
	v_pk_fma_f32 v[152:153], v[108:109], v[96:97], v[152:153] op_sel_hi:[1,0,1]
	v_pk_fma_f32 v[156:157], v[108:109], v[98:99], v[156:157] op_sel_hi:[1,0,1]
	v_pk_fma_f32 v[102:103], v[108:109], v[98:99], v[102:103] op_sel:[0,1,0]
	v_pk_fma_f32 v[106:107], v[108:109], v[100:101], v[106:107] op_sel_hi:[1,0,1]
	v_pk_fma_f32 v[104:105], v[108:109], v[82:83], v[104:105] op_sel_hi:[1,0,1]
	ds_read_b128 v[82:85], v37 offset:25600
	ds_read_b128 v[90:93], v37 offset:25616
	ds_read_b128 v[94:97], v37 offset:25632
	ds_read_b128 v[98:101], v37 offset:25648
	v_mov_b32_e32 v88, v87
	s_waitcnt lgkmcnt(3)
	v_pk_fma_f32 v[108:109], v[88:89], v[82:83], v[110:111] op_sel_hi:[1,0,1]
	v_pk_fma_f32 v[110:111], v[88:89], v[82:83], v[112:113] op_sel:[0,1,0]
	v_mov_b32_e32 v82, v85
	v_pk_fma_f32 v[112:113], v[88:89], v[84:85], v[114:115] op_sel_hi:[1,0,1]
	v_pk_fma_f32 v[114:115], v[88:89], v[82:83], v[116:117] op_sel_hi:[1,0,1]
	s_waitcnt lgkmcnt(2)
	v_mov_b32_e32 v82, v93
	v_pk_fma_f32 v[116:117], v[88:89], v[90:91], v[140:141] op_sel_hi:[1,0,1]
	v_pk_fma_f32 v[140:141], v[88:89], v[90:91], v[142:143] op_sel:[0,1,0]
	v_pk_fma_f32 v[142:143], v[88:89], v[92:93], v[144:145] op_sel_hi:[1,0,1]
	v_pk_fma_f32 v[144:145], v[88:89], v[82:83], v[146:147] op_sel_hi:[1,0,1]
	s_waitcnt lgkmcnt(1)
	v_mov_b32_e32 v82, v97
	v_pk_fma_f32 v[146:147], v[88:89], v[94:95], v[148:149] op_sel_hi:[1,0,1]
	v_pk_fma_f32 v[148:149], v[88:89], v[94:95], v[150:151] op_sel:[0,1,0]
	v_pk_fma_f32 v[150:151], v[88:89], v[96:97], v[152:153] op_sel_hi:[1,0,1]
	v_pk_fma_f32 v[152:153], v[88:89], v[82:83], v[154:155] op_sel_hi:[1,0,1]
	s_waitcnt lgkmcnt(0)
	v_mov_b32_e32 v82, v101
	v_pk_fma_f32 v[154:155], v[88:89], v[98:99], v[156:157] op_sel_hi:[1,0,1]
	v_pk_fma_f32 v[98:99], v[88:89], v[98:99], v[102:103] op_sel:[0,1,0]
	v_pk_fma_f32 v[102:103], v[88:89], v[100:101], v[106:107] op_sel_hi:[1,0,1]
	v_pk_fma_f32 v[100:101], v[88:89], v[82:83], v[104:105] op_sel_hi:[1,0,1]
	ds_read_b128 v[82:85], v37 offset:46080
	ds_read_b128 v[86:89], v37 offset:46096
	ds_read_b128 v[90:93], v37 offset:46112
	ds_read_b128 v[94:97], v37 offset:46128
	v_mov_b32_e32 v104, v16
	v_mov_b32_e32 v105, v76
	s_waitcnt lgkmcnt(3)
	v_mov_b32_e32 v16, v85
	v_pk_fma_f32 v[106:107], v[104:105], v[82:83], v[108:109] op_sel_hi:[1,0,1]
	v_pk_fma_f32 v[108:109], v[104:105], v[82:83], v[110:111] op_sel:[0,1,0]
	v_pk_fma_f32 v[110:111], v[104:105], v[84:85], v[112:113] op_sel_hi:[1,0,1]
	v_pk_fma_f32 v[112:113], v[104:105], v[16:17], v[114:115] op_sel_hi:[1,0,1]
	s_waitcnt lgkmcnt(2)
	v_mov_b32_e32 v16, v89
	v_pk_fma_f32 v[114:115], v[104:105], v[86:87], v[116:117] op_sel_hi:[1,0,1]
	v_pk_fma_f32 v[116:117], v[104:105], v[86:87], v[140:141] op_sel:[0,1,0]
	v_pk_fma_f32 v[140:141], v[104:105], v[88:89], v[142:143] op_sel_hi:[1,0,1]
	v_pk_fma_f32 v[142:143], v[104:105], v[16:17], v[144:145] op_sel_hi:[1,0,1]
	s_waitcnt lgkmcnt(1)
	v_mov_b32_e32 v16, v93
	v_pk_fma_f32 v[144:145], v[104:105], v[90:91], v[146:147] op_sel_hi:[1,0,1]
	v_pk_fma_f32 v[146:147], v[104:105], v[90:91], v[148:149] op_sel:[0,1,0]
	v_pk_fma_f32 v[148:149], v[104:105], v[92:93], v[150:151] op_sel_hi:[1,0,1]
	v_pk_fma_f32 v[150:151], v[104:105], v[16:17], v[152:153] op_sel_hi:[1,0,1]
	s_waitcnt lgkmcnt(0)
	v_mov_b32_e32 v16, v97
	v_pk_fma_f32 v[152:153], v[104:105], v[94:95], v[154:155] op_sel_hi:[1,0,1]
	v_pk_fma_f32 v[98:99], v[104:105], v[94:95], v[98:99] op_sel:[0,1,0]
	v_pk_fma_f32 v[102:103], v[104:105], v[96:97], v[102:103] op_sel_hi:[1,0,1]
	v_pk_fma_f32 v[100:101], v[104:105], v[16:17], v[100:101] op_sel_hi:[1,0,1]
	v_add_u32_e32 v16, 0x10400, v37
	v_add_u32_e32 v76, 0x10410, v37
	ds_read_b128 v[82:85], v16
	ds_read_b128 v[86:89], v76
	v_add_u32_e32 v16, 0x10420, v37
	v_add_u32_e32 v76, 0x10430, v37
	ds_read_b128 v[90:93], v16
	ds_read_b128 v[94:97], v76
	v_mov_b32_e32 v76, v17
	s_waitcnt lgkmcnt(3)
	v_pk_fma_f32 v[16:17], v[76:77], v[82:83], v[106:107] op_sel_hi:[1,0,1]
	v_pk_fma_f32 v[104:105], v[76:77], v[82:83], v[108:109] op_sel:[0,1,0]
	v_mov_b32_e32 v82, v85
	v_pk_fma_f32 v[108:109], v[76:77], v[82:83], v[112:113] op_sel_hi:[1,0,1]
	s_waitcnt lgkmcnt(2)
	v_mov_b32_e32 v82, v89
	v_pk_fma_f32 v[112:113], v[76:77], v[86:87], v[116:117] op_sel:[0,1,0]
	v_pk_fma_f32 v[116:117], v[76:77], v[82:83], v[142:143] op_sel_hi:[1,0,1]
	s_waitcnt lgkmcnt(1)
	v_mov_b32_e32 v82, v93
	v_pk_fma_f32 v[142:143], v[76:77], v[90:91], v[146:147] op_sel:[0,1,0]
	v_pk_fma_f32 v[146:147], v[76:77], v[82:83], v[150:151] op_sel_hi:[1,0,1]
	s_waitcnt lgkmcnt(0)
	v_mov_b32_e32 v82, v97
	v_pk_fma_f32 v[106:107], v[76:77], v[84:85], v[110:111] op_sel_hi:[1,0,1]
	v_pk_fma_f32 v[110:111], v[76:77], v[86:87], v[114:115] op_sel_hi:[1,0,1]
	v_pk_fma_f32 v[114:115], v[76:77], v[88:89], v[140:141] op_sel_hi:[1,0,1]
	v_pk_fma_f32 v[140:141], v[76:77], v[90:91], v[144:145] op_sel_hi:[1,0,1]
	v_pk_fma_f32 v[144:145], v[76:77], v[92:93], v[148:149] op_sel_hi:[1,0,1]
	v_pk_fma_f32 v[148:149], v[76:77], v[94:95], v[152:153] op_sel_hi:[1,0,1]
	v_pk_fma_f32 v[98:99], v[76:77], v[94:95], v[98:99] op_sel:[0,1,0]
	v_pk_fma_f32 v[102:103], v[76:77], v[96:97], v[102:103] op_sel_hi:[1,0,1]
	v_pk_fma_f32 v[76:77], v[76:77], v[82:83], v[100:101] op_sel_hi:[1,0,1]
	ds_read_b128 v[82:85], v37 offset:10240
	ds_read_b128 v[86:89], v37 offset:10256
	ds_read_b128 v[90:93], v37 offset:10272
	ds_read_b128 v[94:97], v37 offset:10288
	v_mov_b32_e32 v100, v78
	v_mov_b32_e32 v101, v80
	s_waitcnt lgkmcnt(3)
	v_mov_b32_e32 v78, v85
	v_pk_fma_f32 v[108:109], v[100:101], v[78:79], v[108:109] op_sel_hi:[1,0,1]
	s_waitcnt lgkmcnt(2)
	v_mov_b32_e32 v78, v89
	v_pk_fma_f32 v[116:117], v[100:101], v[78:79], v[116:117] op_sel_hi:[1,0,1]
	s_waitcnt lgkmcnt(1)
	v_mov_b32_e32 v78, v93
	v_pk_fma_f32 v[146:147], v[100:101], v[78:79], v[146:147] op_sel_hi:[1,0,1]
	s_waitcnt lgkmcnt(0)
	v_mov_b32_e32 v78, v97
	v_pk_fma_f32 v[16:17], v[100:101], v[82:83], v[16:17] op_sel_hi:[1,0,1]
	v_pk_fma_f32 v[76:77], v[100:101], v[78:79], v[76:77] op_sel_hi:[1,0,1]
	v_pk_fma_f32 v[104:105], v[100:101], v[82:83], v[104:105] op_sel:[0,1,0]
	v_pk_fma_f32 v[106:107], v[100:101], v[84:85], v[106:107] op_sel_hi:[1,0,1]
	v_pk_fma_f32 v[110:111], v[100:101], v[86:87], v[110:111] op_sel_hi:[1,0,1]
	v_pk_fma_f32 v[112:113], v[100:101], v[86:87], v[112:113] op_sel:[0,1,0]
	v_pk_fma_f32 v[114:115], v[100:101], v[88:89], v[114:115] op_sel_hi:[1,0,1]
	v_pk_fma_f32 v[140:141], v[100:101], v[90:91], v[140:141] op_sel_hi:[1,0,1]
	v_pk_fma_f32 v[142:143], v[100:101], v[90:91], v[142:143] op_sel:[0,1,0]
	v_pk_fma_f32 v[144:145], v[100:101], v[92:93], v[144:145] op_sel_hi:[1,0,1]
	v_pk_fma_f32 v[148:149], v[100:101], v[94:95], v[148:149] op_sel_hi:[1,0,1]
	v_pk_fma_f32 v[98:99], v[100:101], v[94:95], v[98:99] op_sel:[0,1,0]
	v_pk_fma_f32 v[102:103], v[100:101], v[96:97], v[102:103] op_sel_hi:[1,0,1]
	ds_read_b128 v[82:85], v37 offset:30720
	ds_read_b128 v[86:89], v37 offset:30736
	ds_read_b128 v[90:93], v37 offset:30752
	ds_read_b128 v[94:97], v37 offset:30768
	v_mov_b32_e32 v80, v79
	s_waitcnt lgkmcnt(3)
	v_mov_b32_e32 v78, v85
	v_pk_fma_f32 v[100:101], v[80:81], v[82:83], v[104:105] op_sel:[0,1,0]
	v_pk_fma_f32 v[104:105], v[80:81], v[84:85], v[106:107] op_sel_hi:[1,0,1]
	v_pk_fma_f32 v[106:107], v[80:81], v[78:79], v[108:109] op_sel_hi:[1,0,1]
	s_waitcnt lgkmcnt(2)
	v_mov_b32_e32 v78, v89
	v_pk_fma_f32 v[108:109], v[80:81], v[86:87], v[110:111] op_sel_hi:[1,0,1]
	v_pk_fma_f32 v[110:111], v[80:81], v[86:87], v[112:113] op_sel:[0,1,0]
	v_pk_fma_f32 v[112:113], v[80:81], v[88:89], v[114:115] op_sel_hi:[1,0,1]
	v_pk_fma_f32 v[114:115], v[80:81], v[78:79], v[116:117] op_sel_hi:[1,0,1]
	s_waitcnt lgkmcnt(1)
	v_mov_b32_e32 v78, v93
	v_pk_fma_f32 v[16:17], v[80:81], v[82:83], v[16:17] op_sel_hi:[1,0,1]
	v_pk_fma_f32 v[116:117], v[80:81], v[90:91], v[140:141] op_sel_hi:[1,0,1]
	v_pk_fma_f32 v[140:141], v[80:81], v[90:91], v[142:143] op_sel:[0,1,0]
	v_pk_fma_f32 v[142:143], v[80:81], v[92:93], v[144:145] op_sel_hi:[1,0,1]
	v_pk_fma_f32 v[92:93], v[80:81], v[78:79], v[146:147] op_sel_hi:[1,0,1]
	s_waitcnt lgkmcnt(0)
	v_mov_b32_e32 v78, v97
	v_pk_fma_f32 v[144:145], v[80:81], v[94:95], v[148:149] op_sel_hi:[1,0,1]
	v_pk_fma_f32 v[94:95], v[80:81], v[94:95], v[98:99] op_sel:[0,1,0]
	v_pk_fma_f32 v[98:99], v[80:81], v[96:97], v[102:103] op_sel_hi:[1,0,1]
	v_pk_fma_f32 v[96:97], v[80:81], v[78:79], v[76:77] op_sel_hi:[1,0,1]
	ds_read_b128 v[76:79], v37 offset:51200
	ds_read_b128 v[80:83], v37 offset:51216
	ds_read_b128 v[84:87], v37 offset:51232
	ds_read_b128 v[88:91], v37 offset:51248
	v_mov_b32_e32 v102, v8
	v_mov_b32_e32 v103, v12
	s_waitcnt lgkmcnt(3)
	v_mov_b32_e32 v8, v79
	v_pk_fma_f32 v[106:107], v[102:103], v[8:9], v[106:107] op_sel_hi:[1,0,1]
	s_waitcnt lgkmcnt(2)
	v_mov_b32_e32 v8, v83
	v_pk_fma_f32 v[114:115], v[102:103], v[8:9], v[114:115] op_sel_hi:[1,0,1]
	s_waitcnt lgkmcnt(1)
	v_mov_b32_e32 v8, v87
	v_pk_fma_f32 v[16:17], v[102:103], v[76:77], v[16:17] op_sel_hi:[1,0,1]
	v_pk_fma_f32 v[92:93], v[102:103], v[8:9], v[92:93] op_sel_hi:[1,0,1]
	s_waitcnt lgkmcnt(0)
	v_mov_b32_e32 v8, v91
	v_pk_fma_f32 v[100:101], v[102:103], v[76:77], v[100:101] op_sel:[0,1,0]
	v_pk_fma_f32 v[104:105], v[102:103], v[78:79], v[104:105] op_sel_hi:[1,0,1]
	v_pk_fma_f32 v[108:109], v[102:103], v[80:81], v[108:109] op_sel_hi:[1,0,1]
	v_pk_fma_f32 v[110:111], v[102:103], v[80:81], v[110:111] op_sel:[0,1,0]
	v_pk_fma_f32 v[112:113], v[102:103], v[82:83], v[112:113] op_sel_hi:[1,0,1]
	v_pk_fma_f32 v[116:117], v[102:103], v[84:85], v[116:117] op_sel_hi:[1,0,1]
	v_pk_fma_f32 v[140:141], v[102:103], v[84:85], v[140:141] op_sel:[0,1,0]
	v_pk_fma_f32 v[142:143], v[102:103], v[86:87], v[142:143] op_sel_hi:[1,0,1]
	v_pk_fma_f32 v[144:145], v[102:103], v[88:89], v[144:145] op_sel_hi:[1,0,1]
	v_pk_fma_f32 v[94:95], v[102:103], v[88:89], v[94:95] op_sel:[0,1,0]
	v_pk_fma_f32 v[98:99], v[102:103], v[90:91], v[98:99] op_sel_hi:[1,0,1]
	v_pk_fma_f32 v[96:97], v[102:103], v[8:9], v[96:97] op_sel_hi:[1,0,1]
	v_add_u32_e32 v8, 0x11800, v37
	v_add_u32_e32 v12, 0x11810, v37
	ds_read_b128 v[76:79], v8
	ds_read_b128 v[80:83], v12
	v_add_u32_e32 v8, 0x11820, v37
	v_add_u32_e32 v12, 0x11830, v37
	ds_read_b128 v[84:87], v8
	ds_read_b128 v[88:91], v12
	v_mov_b32_e32 v12, v9
	s_waitcnt lgkmcnt(3)
	v_pk_fma_f32 v[8:9], v[12:13], v[76:77], v[16:17] op_sel_hi:[1,0,1]
	v_pk_fma_f32 v[16:17], v[12:13], v[76:77], v[100:101] op_sel:[0,1,0]
	v_mov_b32_e32 v76, v79
	v_pk_fma_f32 v[102:103], v[12:13], v[76:77], v[106:107] op_sel_hi:[1,0,1]
	s_waitcnt lgkmcnt(2)
	v_mov_b32_e32 v76, v83
	v_pk_fma_f32 v[106:107], v[12:13], v[80:81], v[110:111] op_sel:[0,1,0]
	v_pk_fma_f32 v[110:111], v[12:13], v[76:77], v[114:115] op_sel_hi:[1,0,1]
	s_waitcnt lgkmcnt(1)
	v_mov_b32_e32 v76, v87
	v_pk_fma_f32 v[92:93], v[12:13], v[76:77], v[92:93] op_sel_hi:[1,0,1]
	s_waitcnt lgkmcnt(0)
	v_mov_b32_e32 v76, v91
	v_pk_fma_f32 v[100:101], v[12:13], v[78:79], v[104:105] op_sel_hi:[1,0,1]
	v_pk_fma_f32 v[104:105], v[12:13], v[80:81], v[108:109] op_sel_hi:[1,0,1]
	v_pk_fma_f32 v[108:109], v[12:13], v[82:83], v[112:113] op_sel_hi:[1,0,1]
	v_pk_fma_f32 v[112:113], v[12:13], v[84:85], v[116:117] op_sel_hi:[1,0,1]
	v_pk_fma_f32 v[114:115], v[12:13], v[84:85], v[140:141] op_sel:[0,1,0]
	v_pk_fma_f32 v[116:117], v[12:13], v[86:87], v[142:143] op_sel_hi:[1,0,1]
	v_pk_fma_f32 v[140:141], v[12:13], v[88:89], v[144:145] op_sel_hi:[1,0,1]
	v_pk_fma_f32 v[94:95], v[12:13], v[88:89], v[94:95] op_sel:[0,1,0]
	v_pk_fma_f32 v[98:99], v[12:13], v[90:91], v[98:99] op_sel_hi:[1,0,1]
	v_pk_fma_f32 v[12:13], v[12:13], v[76:77], v[96:97] op_sel_hi:[1,0,1]
	ds_read_b128 v[76:79], v37 offset:15360
	ds_read_b128 v[80:83], v37 offset:15376
	ds_read_b128 v[84:87], v37 offset:15392
	ds_read_b128 v[88:91], v37 offset:15408
	v_mov_b32_e32 v96, v10
	v_mov_b32_e32 v97, v14
	s_waitcnt lgkmcnt(3)
	v_mov_b32_e32 v10, v79
	v_pk_fma_f32 v[102:103], v[96:97], v[10:11], v[102:103] op_sel_hi:[1,0,1]
	s_waitcnt lgkmcnt(2)
	v_mov_b32_e32 v10, v83
	v_pk_fma_f32 v[110:111], v[96:97], v[10:11], v[110:111] op_sel_hi:[1,0,1]
	s_waitcnt lgkmcnt(1)
	v_mov_b32_e32 v10, v87
	v_pk_fma_f32 v[92:93], v[96:97], v[10:11], v[92:93] op_sel_hi:[1,0,1]
	s_waitcnt lgkmcnt(0)
	v_mov_b32_e32 v10, v91
	v_pk_fma_f32 v[8:9], v[96:97], v[76:77], v[8:9] op_sel_hi:[1,0,1]
	v_pk_fma_f32 v[16:17], v[96:97], v[76:77], v[16:17] op_sel:[0,1,0]
	v_pk_fma_f32 v[12:13], v[96:97], v[10:11], v[12:13] op_sel_hi:[1,0,1]
	v_pk_fma_f32 v[100:101], v[96:97], v[78:79], v[100:101] op_sel_hi:[1,0,1]
	v_pk_fma_f32 v[104:105], v[96:97], v[80:81], v[104:105] op_sel_hi:[1,0,1]
	v_pk_fma_f32 v[106:107], v[96:97], v[80:81], v[106:107] op_sel:[0,1,0]
	v_pk_fma_f32 v[108:109], v[96:97], v[82:83], v[108:109] op_sel_hi:[1,0,1]
	v_pk_fma_f32 v[112:113], v[96:97], v[84:85], v[112:113] op_sel_hi:[1,0,1]
	v_pk_fma_f32 v[114:115], v[96:97], v[84:85], v[114:115] op_sel:[0,1,0]
	v_pk_fma_f32 v[116:117], v[96:97], v[86:87], v[116:117] op_sel_hi:[1,0,1]
	v_pk_fma_f32 v[140:141], v[96:97], v[88:89], v[140:141] op_sel_hi:[1,0,1]
	v_pk_fma_f32 v[94:95], v[96:97], v[88:89], v[94:95] op_sel:[0,1,0]
	v_pk_fma_f32 v[98:99], v[96:97], v[90:91], v[98:99] op_sel_hi:[1,0,1]
	ds_read_b128 v[76:79], v37 offset:35840
	ds_read_b128 v[80:83], v37 offset:35856
	ds_read_b128 v[84:87], v37 offset:35872
	ds_read_b128 v[88:91], v37 offset:35888
	v_mov_b32_e32 v14, v11
	s_waitcnt lgkmcnt(3)
	v_pk_fma_f32 v[96:97], v[14:15], v[76:77], v[8:9] op_sel_hi:[1,0,1]
	v_mov_b32_e32 v8, v79
	v_pk_fma_f32 v[102:103], v[14:15], v[8:9], v[102:103] op_sel_hi:[1,0,1]
	s_waitcnt lgkmcnt(2)
	v_mov_b32_e32 v8, v83
	v_pk_fma_f32 v[110:111], v[14:15], v[8:9], v[110:111] op_sel_hi:[1,0,1]
	s_waitcnt lgkmcnt(1)
	v_mov_b32_e32 v8, v87
	v_pk_fma_f32 v[112:113], v[14:15], v[84:85], v[112:113] op_sel_hi:[1,0,1]
	v_pk_fma_f32 v[84:85], v[14:15], v[84:85], v[114:115] op_sel:[0,1,0]
	v_pk_fma_f32 v[114:115], v[14:15], v[86:87], v[116:117] op_sel_hi:[1,0,1]
	v_pk_fma_f32 v[86:87], v[14:15], v[8:9], v[92:93] op_sel_hi:[1,0,1]
	s_waitcnt lgkmcnt(0)
	v_mov_b32_e32 v8, v91
	v_pk_fma_f32 v[16:17], v[14:15], v[76:77], v[16:17] op_sel:[0,1,0]
	v_pk_fma_f32 v[92:93], v[14:15], v[88:89], v[140:141] op_sel_hi:[1,0,1]
	v_pk_fma_f32 v[88:89], v[14:15], v[88:89], v[94:95] op_sel:[0,1,0]
	v_pk_fma_f32 v[94:95], v[14:15], v[90:91], v[98:99] op_sel_hi:[1,0,1]
	v_pk_fma_f32 v[90:91], v[14:15], v[8:9], v[12:13] op_sel_hi:[1,0,1]
	v_pk_fma_f32 v[100:101], v[14:15], v[78:79], v[100:101] op_sel_hi:[1,0,1]
	v_pk_fma_f32 v[104:105], v[14:15], v[80:81], v[104:105] op_sel_hi:[1,0,1]
	v_pk_fma_f32 v[106:107], v[14:15], v[80:81], v[106:107] op_sel:[0,1,0]
	v_pk_fma_f32 v[108:109], v[14:15], v[82:83], v[108:109] op_sel_hi:[1,0,1]
	ds_read_b128 v[8:11], v37 offset:56320
	ds_read_b128 v[12:15], v37 offset:56336
	ds_read_b128 v[76:79], v37 offset:56352
	ds_read_b128 v[80:83], v37 offset:56368
	v_mov_b32_e32 v98, v4
	v_mov_b32_e32 v99, v6
	s_waitcnt lgkmcnt(3)
	v_mov_b32_e32 v4, v11
	v_pk_fma_f32 v[102:103], v[98:99], v[4:5], v[102:103] op_sel_hi:[1,0,1]
	s_waitcnt lgkmcnt(2)
	v_mov_b32_e32 v4, v15
	v_pk_fma_f32 v[110:111], v[98:99], v[4:5], v[110:111] op_sel_hi:[1,0,1]
	s_waitcnt lgkmcnt(1)
	v_mov_b32_e32 v4, v79
	v_pk_fma_f32 v[16:17], v[98:99], v[8:9], v[16:17] op_sel:[0,1,0]
	v_pk_fma_f32 v[84:85], v[98:99], v[76:77], v[84:85] op_sel:[0,1,0]
	v_pk_fma_f32 v[140:141], v[98:99], v[4:5], v[86:87] op_sel_hi:[1,0,1]
	s_waitcnt lgkmcnt(0)
	v_mov_b32_e32 v4, v83
	v_pk_fma_f32 v[116:117], v[98:99], v[8:9], v[96:97] op_sel_hi:[1,0,1]
	v_pk_fma_f32 v[100:101], v[98:99], v[10:11], v[100:101] op_sel_hi:[1,0,1]
	v_pk_fma_f32 v[104:105], v[98:99], v[12:13], v[104:105] op_sel_hi:[1,0,1]
	v_pk_fma_f32 v[106:107], v[98:99], v[12:13], v[106:107] op_sel:[0,1,0]
	v_pk_fma_f32 v[108:109], v[98:99], v[14:15], v[108:109] op_sel_hi:[1,0,1]
	v_pk_fma_f32 v[112:113], v[98:99], v[76:77], v[112:113] op_sel_hi:[1,0,1]
	v_pk_fma_f32 v[114:115], v[98:99], v[78:79], v[114:115] op_sel_hi:[1,0,1]
	v_pk_fma_f32 v[142:143], v[98:99], v[80:81], v[92:93] op_sel_hi:[1,0,1]
	v_pk_fma_f32 v[144:145], v[98:99], v[80:81], v[88:89] op_sel:[0,1,0]
	v_pk_fma_f32 v[146:147], v[98:99], v[82:83], v[94:95] op_sel_hi:[1,0,1]
	v_pk_fma_f32 v[98:99], v[98:99], v[4:5], v[90:91] op_sel_hi:[1,0,1]
	v_add_u32_e32 v4, 0x12c00, v37
	v_add_u32_e32 v6, 0x12c10, v37
	ds_read_b128 v[8:11], v4
	ds_read_b128 v[80:83], v6
	v_add_u32_e32 v4, 0x12c20, v37
	v_add_u32_e32 v6, 0x12c30, v37
	ds_read_b128 v[88:91], v4
	ds_read_b128 v[94:97], v6
	v_mov_b32_e32 v6, v5
	s_waitcnt lgkmcnt(3)
	v_mov_b32_e32 v4, v11
	v_pk_fma_f32 v[76:77], v[6:7], v[4:5], v[102:103] op_sel_hi:[1,0,1]
	s_waitcnt lgkmcnt(2)
	v_pk_fma_f32 v[12:13], v[6:7], v[80:81], v[104:105] op_sel_hi:[1,0,1]
	v_pk_fma_f32 v[4:5], v[6:7], v[80:81], v[106:107] op_sel:[0,1,0]
	s_waitcnt lgkmcnt(1)
	v_mov_b32_e32 v80, v91
	v_pk_fma_f32 v[14:15], v[6:7], v[8:9], v[16:17] op_sel:[0,1,0]
	v_pk_fma_f32 v[16:17], v[6:7], v[10:11], v[100:101] op_sel_hi:[1,0,1]
	v_mov_b32_e32 v10, v83
	v_pk_fma_f32 v[92:93], v[6:7], v[88:89], v[112:113] op_sel_hi:[1,0,1]
	v_pk_fma_f32 v[86:87], v[6:7], v[88:89], v[84:85] op_sel:[0,1,0]
	v_pk_fma_f32 v[88:89], v[6:7], v[90:91], v[114:115] op_sel_hi:[1,0,1]
	v_pk_fma_f32 v[90:91], v[6:7], v[80:81], v[140:141] op_sel_hi:[1,0,1]
	s_waitcnt lgkmcnt(0)
	v_pk_fma_f32 v[84:85], v[6:7], v[94:95], v[142:143] op_sel_hi:[1,0,1]
	v_pk_fma_f32 v[80:81], v[6:7], v[94:95], v[144:145] op_sel:[0,1,0]
	v_mov_b32_e32 v94, v97
	v_pk_fma_f32 v[78:79], v[6:7], v[8:9], v[116:117] op_sel_hi:[1,0,1]
	v_pk_fma_f32 v[8:9], v[6:7], v[82:83], v[108:109] op_sel_hi:[1,0,1]
	v_pk_fma_f32 v[10:11], v[6:7], v[10:11], v[110:111] op_sel_hi:[1,0,1]
	v_pk_fma_f32 v[82:83], v[6:7], v[96:97], v[146:147] op_sel_hi:[1,0,1]
	v_pk_fma_f32 v[6:7], v[6:7], v[94:95], v[98:99] op_sel_hi:[1,0,1]
	s_nop 0
	s_nop 0
	s_nop 4
	v_permlane32_swap_b32_e32 v78, v92
	v_permlane32_swap_b32_e32 v14, v86
	v_permlane32_swap_b32_e32 v16, v88
	v_permlane32_swap_b32_e32 v76, v90
	v_permlane32_swap_b32_e32 v12, v84
	v_permlane32_swap_b32_e32 v4, v80
	v_permlane32_swap_b32_e32 v8, v82
	v_permlane32_swap_b32_e32 v10, v6
	v_add_f32_e32 v37, v92, v78
	v_add_f32_e32 v14, v86, v14
	v_add_f32_e32 v16, v88, v16
	v_add_f32_e32 v76, v90, v76
	v_add_f32_e32 v12, v84, v12
	v_add_f32_e32 v4, v80, v4
	v_add_f32_e32 v8, v82, v8
	v_add_f32_e32 v6, v6, v10
	s_nop 1
	v_permlane16_swap_b32_e32 v37, v12
	v_permlane16_swap_b32_e32 v14, v4
	v_permlane16_swap_b32_e32 v16, v8
	v_permlane16_swap_b32_e32 v76, v6
	v_add_f32_e32 v10, v12, v37
	v_add_f32_e32 v4, v4, v14
	v_add_f32_e32 v8, v8, v16
	v_add_f32_e32 v6, v6, v76
	v_cndmask_b32_e64 v12, v8, v10, s[10:11]
	v_cndmask_b32_e64 v8, v10, v8, s[10:11]
	v_cndmask_b32_e64 v10, v6, v4, s[10:11]
	v_cndmask_b32_e64 v4, v4, v6, s[10:11]
	s_nop 1
	v_add_f32_dpp v8, v8, v12 row_ror:8 row_mask:0xf bank_mask:0xf
	v_add_f32_dpp v4, v4, v10 row_ror:8 row_mask:0xf bank_mask:0xf
	v_cndmask_b32_e64 v6, v4, v8, s[12:13]
	v_cndmask_b32_e64 v4, v8, v4, s[12:13]
	s_nop 1
	v_add_f32_dpp v164, v4, v6 row_shl:4 row_mask:0xf bank_mask:0x5
	v_add_f32_dpp v164, v4, v6 row_shr:4 row_mask:0xf bank_mask:0xa
	s_nop 1
	v_add_f32_dpp v165, v164, v164 quad_perm:[2,3,0,1] row_mask:0xf bank_mask:0xf
	s_nop 1
	v_add_f32_dpp v4, v165, v165 quad_perm:[1,0,3,2] row_mask:0xf bank_mask:0xf
	v_mov_b32_e32 v164, v4
	v_mov_b32_e32 v165, v4
	s_nop 1
	v_permlane32_swap_b32_e32 v164, v165
	v_max_f32_e32 v6, v164, v165
	v_mov_b32_e32 v164, v6
	v_mov_b32_e32 v165, v6
	s_nop 1
	v_permlane16_swap_b32_e32 v164, v165
	v_max_f32_e32 v6, v164, v165
	s_nop 1
	v_max_f32_dpp v6, v6, v6 row_ror:8 row_mask:0xf bank_mask:0xf
	s_nop 1
	v_max_f32_dpp v6, v6, v6 row_half_mirror row_mask:0xf bank_mask:0xf
	v_sub_f32_e32 v4, v4, v6
	v_mul_f32_e32 v6, 0x3fb8aa3b, v4
	v_fma_f32 v8, v4, s33, -v6
	v_rndne_f32_e32 v10, v6
	v_fmac_f32_e32 v8, 0x32a5705f, v4
	v_sub_f32_e32 v6, v6, v10
	v_add_f32_e32 v6, v6, v8
	v_exp_f32_e32 v6, v6
	v_cvt_i32_f32_e32 v8, v10
	v_cmp_ngt_f32_e32 vcc, s36, v4
	v_ldexp_f32 v6, v6, v8
	s_nop 0
	v_cndmask_b32_e32 v6, 0, v6, vcc
	v_cmp_nlt_f32_e32 vcc, s53, v4
	s_nop 1
	v_cndmask_b32_e32 v4, v216, v6, vcc
	v_mov_b32_e32 v164, v4
	v_mov_b32_e32 v165, v4
	s_nop 1
	v_permlane32_swap_b32_e32 v164, v165
	v_add_f32_e32 v6, v164, v165
	v_mov_b32_e32 v164, v6
	v_mov_b32_e32 v165, v6
	s_nop 1
	v_permlane16_swap_b32_e32 v164, v165
	v_add_f32_e32 v6, v164, v165
	s_nop 1
	v_add_f32_dpp v6, v6, v6 row_ror:8 row_mask:0xf bank_mask:0xf
	s_nop 1
	v_add_f32_dpp v6, v6, v6 row_half_mirror row_mask:0xf bank_mask:0xf
	s_and_saveexec_b64 s[16:17], s[14:15]
	s_cbranch_execz .LBB0_1263
	v_div_scale_f32 v8, s[34:35], v6, v6, v4
	v_rcp_f32_e32 v10, v8
	v_div_scale_f32 v12, vcc, v4, v6, v4
	v_lshl_add_u64 v[94:95], s[62:63], 0, v[38:39]
	v_fma_f32 v14, -v8, v10, 1.0
	v_fmac_f32_e32 v10, v14, v10
	v_mul_f32_e32 v14, v12, v10
	v_fma_f32 v16, -v8, v14, v12
	v_fmac_f32_e32 v14, v16, v10
	v_fma_f32 v8, -v8, v14, v12
	v_div_fmas_f32 v8, v8, v10, v14
	v_div_fixup_f32 v4, v8, v6, v4
	global_store_dword v[94:95], v4, off
